# second workgroup barrier replaced by per-wave LDS flags; each wave starts phase B with its own row block
# baseline (speedup 1.0000x reference)
_Z12fused_kernelPKfS0_Pf:
	s_load_dwordx4 s[12:15], s[0:1], 0x0
	s_load_dwordx2 s[8:9], s[0:1], 0x10
	s_lshl_b32 s0, s2, 5
	s_and_b32 s0, s0, 0xe0
	s_lshr_b32 s3, s2, 3
	s_add_i32 s0, s0, s3
	v_and_b32_e32 v1, 63, v0
	v_lshrrev_b32_e32 v200, 6, v0
	s_lshl_b32 s0, s0, 17
	v_lshlrev_b32_e32 v194, 4, v0
	v_lshl_add_u32 v2, v200, 25, s0
	v_lshlrev_b32_e32 v198, 4, v1
	v_add_u32_e32 v106, 0x2000, v194
	v_add_u32_e32 v107, 0x4000, v194
	v_or_b32_e32 v203, v2, v198
	v_lshlrev_b32_e32 v196, 10, v200
	v_mov_b32_e32 v195, 0
	v_or_b32_e32 v233, v203, v196
	s_mov_b32 s7, 0x20000
	s_brev_b32 s6, 8
	s_waitcnt lgkmcnt(0)
	s_and_b32 s5, s13, 0xffff
	s_mov_b32 s4, s12
	buffer_load_dwordx4 v[70:73], v233, s[4:7], 0 offen nt
	v_or_b32_e32 v227, 0x2000, v233
	buffer_load_dwordx4 v[66:69], v227, s[4:7], 0 offen nt
	v_or_b32_e32 v226, 0x4000, v233
	buffer_load_dwordx4 v[78:81], v226, s[4:7], 0 offen nt
	v_or_b32_e32 v227, 0x6000, v233
	buffer_load_dwordx4 v[74:77], v227, s[4:7], 0 offen nt
	v_or_b32_e32 v226, 0x8000, v233
	buffer_load_dwordx4 v[86:89], v226, s[4:7], 0 offen nt
	v_or_b32_e32 v227, 0xa000, v233
	buffer_load_dwordx4 v[82:85], v227, s[4:7], 0 offen nt
	v_or_b32_e32 v226, 0xc000, v233
	buffer_load_dwordx4 v[94:97], v226, s[4:7], 0 offen nt
	v_or_b32_e32 v227, 0xe000, v233
	buffer_load_dwordx4 v[90:93], v227, s[4:7], 0 offen nt
	v_or_b32_e32 v226, 0x10000, v233
	buffer_load_dwordx4 v[150:153], v226, s[4:7], 0 offen nt
	v_or_b32_e32 v227, 0x12000, v233
	buffer_load_dwordx4 v[146:149], v227, s[4:7], 0 offen nt
	v_or_b32_e32 v226, 0x14000, v233
	buffer_load_dwordx4 v[162:165], v226, s[4:7], 0 offen nt
	v_or_b32_e32 v227, 0x16000, v233
	buffer_load_dwordx4 v[154:157], v227, s[4:7], 0 offen nt
	v_or_b32_e32 v226, 0x18000, v233
	buffer_load_dwordx4 v[174:177], v226, s[4:7], 0 offen nt
	v_or_b32_e32 v227, 0x1a000, v233
	buffer_load_dwordx4 v[166:169], v227, s[4:7], 0 offen nt
	v_or_b32_e32 v226, 0x1c000, v233
	buffer_load_dwordx4 v[182:185], v226, s[4:7], 0 offen nt
	v_or_b32_e32 v227, 0x1e000, v233
	buffer_load_dwordx4 v[178:181], v227, s[4:7], 0 offen nt
	global_load_dwordx4 v[228:231], v194, s[14:15]
	global_load_dwordx4 v[98:101], v106, s[14:15]
	global_load_dwordx4 v[102:105], v107, s[14:15]
	v_add_u32_e32 v107, 0x6000, v194
	global_load_dwordx4 v[116:119], v107, s[14:15]
	v_add_u32_e32 v106, 0x8000, v194
	global_load_dwordx4 v[120:123], v106, s[14:15]
	v_add_u32_e32 v107, 0xa000, v194
	global_load_dwordx4 v[124:127], v107, s[14:15]
	v_add_u32_e32 v106, 0xc000, v194
	global_load_dwordx4 v[128:131], v106, s[14:15]
	v_add_u32_e32 v107, 0xe000, v194
	global_load_dwordx4 v[132:135], v107, s[14:15]
	v_add_u32_e32 v106, 0x10000, v194
	global_load_dwordx4 v[136:139], v106, s[14:15]
	v_add_u32_e32 v107, 0x12000, v194
	global_load_dwordx4 v[140:143], v107, s[14:15]
	v_add_u32_e32 v106, 0x14000, v194
	global_load_dwordx4 v[158:161], v106, s[14:15]
	v_add_u32_e32 v107, 0x16000, v194
	global_load_dwordx4 v[170:173], v107, s[14:15]
	v_add_u32_e32 v106, 0x18000, v194
	global_load_dwordx4 v[186:189], v106, s[14:15]
	v_add_u32_e32 v107, 0x1a000, v194
	global_load_dwordx4 v[190:193], v107, s[14:15]
	v_add_u32_e32 v106, 0x1c000, v194
	global_load_dwordx4 v[204:207], v106, s[14:15]
	v_add_u32_e32 v107, 0x1e000, v194
	global_load_dwordx4 v[208:211], v107, s[14:15]
	v_add_u32_e32 v106, 0x20000, v194
	global_load_dwordx4 v[212:215], v106, s[14:15]
	v_add_u32_e32 v107, 0x22000, v194
	global_load_dwordx4 v[216:219], v107, s[14:15]
	v_add_u32_e32 v106, 0x24000, v194
	global_load_dwordx4 v[220:223], v106, s[14:15]
	v_add_u32_e32 v107, 0x26000, v194
	global_load_dwordx4 v[112:115], v107, s[14:15]
	v_add_u32_e32 v224, 0x400, v196
	s_movk_i32 s0, 0x1c00
	v_and_or_b32 v224, v224, s0, v203
	buffer_load_dwordx4 v[62:65], v224, s[4:7], 0 offen nt
	v_or_b32_e32 v227, 0x2000, v224
	buffer_load_dwordx4 v[38:41], v227, s[4:7], 0 offen nt
	v_or_b32_e32 v226, 0x4000, v224
	buffer_load_dwordx4 v[42:45], v226, s[4:7], 0 offen nt
	v_or_b32_e32 v227, 0x6000, v224
	buffer_load_dwordx4 v[14:17], v227, s[4:7], 0 offen nt
	v_or_b32_e32 v226, 0x8000, v224
	buffer_load_dwordx4 v[46:49], v226, s[4:7], 0 offen nt
	v_or_b32_e32 v227, 0xa000, v224
	buffer_load_dwordx4 v[18:21], v227, s[4:7], 0 offen nt
	v_or_b32_e32 v226, 0xc000, v224
	buffer_load_dwordx4 v[50:53], v226, s[4:7], 0 offen nt
	v_or_b32_e32 v227, 0xe000, v224
	buffer_load_dwordx4 v[22:25], v227, s[4:7], 0 offen nt
	v_or_b32_e32 v226, 0x10000, v224
	buffer_load_dwordx4 v[54:57], v226, s[4:7], 0 offen nt
	v_or_b32_e32 v227, 0x12000, v224
	buffer_load_dwordx4 v[26:29], v227, s[4:7], 0 offen nt
	v_or_b32_e32 v226, 0x14000, v224
	buffer_load_dwordx4 v[58:61], v226, s[4:7], 0 offen nt
	v_or_b32_e32 v227, 0x16000, v224
	buffer_load_dwordx4 v[30:33], v227, s[4:7], 0 offen nt
	v_or_b32_e32 v226, 0x18000, v224
	buffer_load_dwordx4 v[34:37], v226, s[4:7], 0 offen nt
	v_or_b32_e32 v227, 0x1a000, v224
	buffer_load_dwordx4 v[6:9], v227, s[4:7], 0 offen nt
	v_or_b32_e32 v226, 0x1c000, v224
	buffer_load_dwordx4 v[10:13], v226, s[4:7], 0 offen nt
	v_or_b32_e32 v227, 0x1e000, v224
	buffer_load_dwordx4 v[2:5], v227, s[4:7], 0 offen nt
	s_mov_b32 s1, 0xe000
	s_mov_b32 s10, 0xa000
	s_mov_b32 s11, 0x6000
	s_mov_b32 s12, 0xc000
	s_mov_b32 s13, 0x8000
	s_mov_b32 s14, 0x1e000
	s_mov_b32 s15, 0x1c000
	s_mov_b32 s16, 0x2000
	s_mov_b32 s17, 0x4000
	s_mov_b32 s18, 0x10000
	s_mov_b32 s19, 0x1a000
	s_mov_b32 s20, 0x18000
	s_mov_b32 s21, 0x16000
	s_mov_b32 s22, 0x14000
	s_mov_b32 s23, 0x12000
	s_mov_b32 s24, 0xe0
	s_mov_b32 s26, 0x3e13bb63
	v_lshrrev_b32_e32 v144, 3, v0
	v_bfe_u32 v145, v0, 1, 2
	v_lshlrev_b32_e32 v108, 3, v0
	v_and_b32_e32 v109, 8, v108
	v_lshlrev_b32_e32 v224, 8, v144
	v_lshlrev_b32_e32 v225, 6, v145
	v_lshlrev_b32_e32 v226, 8, v145
	v_lshlrev_b32_e32 v110, 10, v144
	v_or3_b32 v110, v226, v110, v109
	v_or3_b32 v111, v224, v225, v109
	v_add_u32_e32 v111, 0xff00, v111
	v_add_u32_e32 v144, 0x24800, v194
	v_bfe_u32 v201, v0, 4, 2
	v_and_b32_e32 v197, 15, v0
	v_lshlrev_b32_e32 v202, 2, v201
	s_waitcnt vmcnt(34)
	v_pk_add_f32 v[224:225], v[228:229], 0 op_sel_hi:[1,0]
	v_pk_add_f32 v[226:227], v[230:231], 0 op_sel_hi:[1,0]
	v_cvt_pk_bf16_f32 v228, v228, v229
	v_cvt_pk_bf16_f32 v229, v230, v231
	v_pk_add_f32 v[224:225], v[224:225], v[98:99]
	v_pk_add_f32 v[226:227], v[226:227], v[100:101]
	v_cvt_pk_bf16_f32 v98, v98, v99
	v_cvt_pk_bf16_f32 v99, v100, v101
	ds_write2_b64 v110, v[228:229], v[98:99] offset1:2
	s_waitcnt vmcnt(32)
	v_pk_add_f32 v[224:225], v[224:225], v[102:103]
	v_pk_add_f32 v[226:227], v[226:227], v[104:105]
	v_cvt_pk_bf16_f32 v102, v102, v103
	v_cvt_pk_bf16_f32 v103, v104, v105
	v_pk_add_f32 v[224:225], v[224:225], v[116:117]
	v_pk_add_f32 v[226:227], v[226:227], v[118:119]
	v_cvt_pk_bf16_f32 v116, v116, v117
	v_cvt_pk_bf16_f32 v117, v118, v119
	ds_write2_b64 v110, v[102:103], v[116:117] offset0:4 offset1:6
	s_waitcnt vmcnt(30)
	v_pk_add_f32 v[224:225], v[224:225], v[120:121]
	v_pk_add_f32 v[226:227], v[226:227], v[122:123]
	v_cvt_pk_bf16_f32 v120, v120, v121
	v_cvt_pk_bf16_f32 v121, v122, v123
	v_pk_add_f32 v[224:225], v[224:225], v[124:125]
	v_pk_add_f32 v[226:227], v[226:227], v[126:127]
	v_cvt_pk_bf16_f32 v124, v124, v125
	v_cvt_pk_bf16_f32 v125, v126, v127
	ds_write2_b64 v110, v[120:121], v[124:125] offset0:8 offset1:10
	s_waitcnt vmcnt(28)
	v_pk_add_f32 v[224:225], v[224:225], v[128:129]
	v_pk_add_f32 v[226:227], v[226:227], v[130:131]
	v_cvt_pk_bf16_f32 v128, v128, v129
	v_cvt_pk_bf16_f32 v129, v130, v131
	v_pk_add_f32 v[224:225], v[224:225], v[132:133]
	v_pk_add_f32 v[226:227], v[226:227], v[134:135]
	v_cvt_pk_bf16_f32 v132, v132, v133
	v_cvt_pk_bf16_f32 v133, v134, v135
	ds_write2_b64 v110, v[128:129], v[132:133] offset0:12 offset1:14
	s_waitcnt vmcnt(26)
	v_pk_add_f32 v[224:225], v[224:225], v[136:137]
	v_pk_add_f32 v[226:227], v[226:227], v[138:139]
	v_cvt_pk_bf16_f32 v136, v136, v137
	v_cvt_pk_bf16_f32 v137, v138, v139
	v_pk_add_f32 v[224:225], v[224:225], v[140:141]
	v_pk_add_f32 v[226:227], v[226:227], v[142:143]
	v_cvt_pk_bf16_f32 v140, v140, v141
	v_cvt_pk_bf16_f32 v141, v142, v143
	ds_write2_b64 v110, v[136:137], v[140:141] offset0:16 offset1:18
	s_waitcnt vmcnt(24)
	v_pk_add_f32 v[224:225], v[224:225], v[158:159]
	v_pk_add_f32 v[226:227], v[226:227], v[160:161]
	v_cvt_pk_bf16_f32 v158, v158, v159
	v_cvt_pk_bf16_f32 v159, v160, v161
	v_pk_add_f32 v[224:225], v[224:225], v[170:171]
	v_pk_add_f32 v[226:227], v[226:227], v[172:173]
	v_cvt_pk_bf16_f32 v170, v170, v171
	v_cvt_pk_bf16_f32 v171, v172, v173
	ds_write2_b64 v110, v[158:159], v[170:171] offset0:20 offset1:22
	s_waitcnt vmcnt(22)
	v_pk_add_f32 v[224:225], v[224:225], v[186:187]
	v_pk_add_f32 v[226:227], v[226:227], v[188:189]
	v_cvt_pk_bf16_f32 v186, v186, v187
	v_cvt_pk_bf16_f32 v187, v188, v189
	v_pk_add_f32 v[224:225], v[224:225], v[190:191]
	v_pk_add_f32 v[226:227], v[226:227], v[192:193]
	v_cvt_pk_bf16_f32 v190, v190, v191
	v_cvt_pk_bf16_f32 v191, v192, v193
	ds_write2_b64 v110, v[186:187], v[190:191] offset0:24 offset1:26
	s_waitcnt vmcnt(20)
	v_pk_add_f32 v[224:225], v[224:225], v[204:205]
	v_pk_add_f32 v[226:227], v[226:227], v[206:207]
	v_cvt_pk_bf16_f32 v204, v204, v205
	v_cvt_pk_bf16_f32 v205, v206, v207
	v_pk_add_f32 v[224:225], v[224:225], v[208:209]
	v_pk_add_f32 v[226:227], v[226:227], v[210:211]
	v_cvt_pk_bf16_f32 v208, v208, v209
	v_cvt_pk_bf16_f32 v209, v210, v211
	ds_write2_b64 v110, v[204:205], v[208:209] offset0:28 offset1:30
	s_waitcnt vmcnt(18)
	v_pk_add_f32 v[224:225], v[224:225], v[212:213]
	v_pk_add_f32 v[226:227], v[226:227], v[214:215]
	v_cvt_pk_bf16_f32 v212, v212, v213
	v_cvt_pk_bf16_f32 v213, v214, v215
	v_pk_add_f32 v[224:225], v[224:225], v[216:217]
	v_pk_add_f32 v[226:227], v[226:227], v[218:219]
	v_cvt_pk_bf16_f32 v216, v216, v217
	v_cvt_pk_bf16_f32 v217, v218, v219
	ds_write2_b64 v111, v[212:213], v[216:217] offset0:32 offset1:34
	s_waitcnt vmcnt(16)
	v_pk_add_f32 v[224:225], v[224:225], v[220:221]
	v_pk_add_f32 v[226:227], v[226:227], v[222:223]
	v_cvt_pk_bf16_f32 v220, v220, v221
	v_cvt_pk_bf16_f32 v221, v222, v223
	v_pk_add_f32 v[224:225], v[224:225], v[112:113]
	v_pk_add_f32 v[226:227], v[226:227], v[114:115]
	v_cvt_pk_bf16_f32 v112, v112, v113
	v_cvt_pk_bf16_f32 v113, v114, v115
	ds_write2_b64 v111, v[220:221], v[112:113] offset0:36 offset1:38
	v_pk_mul_f32 v[224:225], v[224:225], s[26:27] op_sel_hi:[1,0]
	v_pk_mul_f32 v[226:227], v[226:227], s[26:27] op_sel_hi:[1,0]
	ds_write_b128 v144, v[224:227]
	v_and_or_b32 v98, v0, 3, v202
	v_mov_b32_e32 v99, 0x10000
	v_lshl_or_b32 v204, v98, 4, v99
	s_movk_i32 s25, 0x2100
	v_mov_b32_e32 v98, 0x14000
	v_mad_u32_u24 v199, v200, s25, v98
	v_add_u32_e32 v98, 0x800, v196
	v_and_or_b32 v186, v98, s0, v203
	v_or_b32_e32 v98, 0x2000, v186
	v_lshlrev_b32_e32 v225, 2, v200
	v_add_u32_e32 v225, 0x26800, v225
	v_mov_b32_e32 v226, 0
	ds_write_b32 v225, v226
	s_waitcnt lgkmcnt(0)
	s_barrier
	buffer_load_dwordx4 v[102:105], v186, s[4:7], 0 offen nt
	s_nop 0
	buffer_load_dwordx4 v[98:101], v98, s[4:7], 0 offen nt
	v_or_b32_e32 v106, 0x4000, v186
	v_or_b32_e32 v107, 0x6000, v186
	v_or_b32_e32 v114, 0x8000, v186
	v_or_b32_e32 v115, 0xa000, v186
	v_or_b32_e32 v122, 0xc000, v186
	v_or_b32_e32 v123, 0xe000, v186
	v_or_b32_e32 v130, 0x10000, v186
	v_or_b32_e32 v131, 0x12000, v186
	v_or_b32_e32 v138, 0x14000, v186
	v_or_b32_e32 v139, 0x16000, v186
	v_or_b32_e32 v158, 0x18000, v186
	v_or_b32_e32 v159, 0x1a000, v186
	v_or_b32_e32 v187, 0x1c000, v186
	v_or_b32_e32 v186, 0x1e000, v186
	v_or_b32_e32 v213, v199, v109
	v_and_b32_e32 v214, 0x1f0, v108
	buffer_load_dwordx4 v[110:113], v106, s[4:7], 0 offen nt
	s_nop 0
	buffer_load_dwordx4 v[106:109], v107, s[4:7], 0 offen nt
	s_nop 0
	buffer_load_dwordx4 v[118:121], v114, s[4:7], 0 offen nt
	s_nop 0
	buffer_load_dwordx4 v[114:117], v115, s[4:7], 0 offen nt
	s_nop 0
	buffer_load_dwordx4 v[126:129], v122, s[4:7], 0 offen nt
	s_nop 0
	buffer_load_dwordx4 v[122:125], v123, s[4:7], 0 offen nt
	s_nop 0
	buffer_load_dwordx4 v[134:137], v130, s[4:7], 0 offen nt
	s_nop 0
	buffer_load_dwordx4 v[130:133], v131, s[4:7], 0 offen nt
	s_nop 0
	buffer_load_dwordx4 v[142:145], v138, s[4:7], 0 offen nt
	s_nop 0
	buffer_load_dwordx4 v[138:141], v139, s[4:7], 0 offen nt
	s_nop 0
	buffer_load_dwordx4 v[170:173], v158, s[4:7], 0 offen nt
	s_nop 0
	buffer_load_dwordx4 v[158:161], v159, s[4:7], 0 offen nt
	s_nop 0
	buffer_load_dwordx4 v[190:193], v187, s[4:7], 0 offen nt
	s_nop 0
	buffer_load_dwordx4 v[186:189], v186, s[4:7], 0 offen nt
	s_waitcnt vmcnt(32)
	v_cvt_pk_bf16_f32 v66, v66, v67
	v_cvt_pk_bf16_f32 v67, v68, v69
	s_movk_i32 s25, 0x50
	v_xad_u32 v207, v214, s25, v213
	s_movk_i32 s25, 0x60
	v_xad_u32 v206, v214, s25, v213
	s_movk_i32 s25, 0x70
	v_xad_u32 v205, v214, s25, v213
	s_movk_i32 s25, 0x80
	v_xad_u32 v211, v214, 16, v213
	v_xad_u32 v231, v214, s25, v213
	s_movk_i32 s25, 0x90
	v_xad_u32 v210, v214, 32, v213
	v_xad_u32 v230, v214, s25, v213
	s_movk_i32 s25, 0xa0
	ds_write_b64 v211, v[66:67] offset:512
	v_cvt_pk_bf16_f32 v66, v78, v79
	v_cvt_pk_bf16_f32 v67, v80, v81
	v_xad_u32 v209, v214, 48, v213
	v_xad_u32 v229, v214, s25, v213
	s_movk_i32 s25, 0xb0
	ds_write_b64 v210, v[66:67] offset:1024
	v_cvt_pk_bf16_f32 v66, v74, v75
	v_cvt_pk_bf16_f32 v67, v76, v77
	v_xad_u32 v208, v214, 64, v213
	v_xad_u32 v228, v214, s25, v213
	s_movk_i32 s25, 0xc0
	ds_write_b64 v209, v[66:67] offset:1536
	v_cvt_pk_bf16_f32 v66, v86, v87
	v_cvt_pk_bf16_f32 v67, v88, v89
	v_xad_u32 v227, v214, s25, v213
	s_movk_i32 s25, 0xd0
	v_xad_u32 v225, v214, s24, v213
	s_movk_i32 s24, 0xf0
	ds_write_b64 v208, v[66:67] offset:2048
	v_cvt_pk_bf16_f32 v66, v82, v83
	v_cvt_pk_bf16_f32 v67, v84, v85
	v_add_u32_e32 v212, v213, v214
	v_xad_u32 v226, v214, s25, v213
	v_xad_u32 v224, v214, s24, v213
	v_lshl_add_u32 v213, v197, 9, v199
	v_bitop3_b32 v214, v201, v0, 15 bitop3:0x78
	ds_write_b64 v207, v[66:67] offset:2560
	v_cvt_pk_bf16_f32 v66, v94, v95
	v_cvt_pk_bf16_f32 v67, v96, v97
	v_lshl_or_b32 v223, v214, 4, v213
	v_bitop3_b32 v214, v201, v197, 4 bitop3:0x36
	ds_write_b64 v206, v[66:67] offset:3072
	v_cvt_pk_bf16_f32 v66, v90, v91
	v_cvt_pk_bf16_f32 v67, v92, v93
	v_lshl_or_b32 v222, v214, 4, v213
	v_bitop3_b32 v214, v201, v197, 8 bitop3:0x36
	ds_write_b64 v205, v[66:67] offset:3584
	v_cvt_pk_bf16_f32 v66, v150, v151
	v_cvt_pk_bf16_f32 v67, v152, v153
	v_lshl_or_b32 v221, v214, 4, v213
	v_bitop3_b32 v214, v201, v197, 12 bitop3:0x36
	ds_write_b64 v231, v[66:67] offset:4096
	v_cvt_pk_bf16_f32 v66, v146, v147
	v_cvt_pk_bf16_f32 v67, v148, v149
	v_lshl_or_b32 v219, v214, 4, v213
	v_bitop3_b32 v214, v201, v197, 16 bitop3:0x36
	ds_write_b64 v230, v[66:67] offset:4608
	v_cvt_pk_bf16_f32 v66, v162, v163
	v_cvt_pk_bf16_f32 v67, v164, v165
	v_lshl_add_u32 v218, v214, 4, v213
	v_bitop3_b32 v214, v201, v197, 20 bitop3:0x36
	ds_write_b64 v229, v[66:67] offset:5120
	v_cvt_pk_bf16_f32 v66, v154, v155
	v_cvt_pk_bf16_f32 v67, v156, v157
	v_lshl_add_u32 v217, v214, 4, v213
	v_bitop3_b32 v214, v201, v197, 24 bitop3:0x36
	ds_write_b64 v228, v[66:67] offset:5632
	v_cvt_pk_bf16_f32 v66, v174, v175
	v_cvt_pk_bf16_f32 v67, v176, v177
	v_lshl_add_u32 v216, v214, 4, v213
	v_bitop3_b32 v214, v201, v197, 28 bitop3:0x36
	ds_write_b64 v227, v[66:67] offset:6144
	v_cvt_pk_bf16_f32 v66, v166, v167
	v_cvt_pk_bf16_f32 v67, v168, v169
	v_add_u32_e32 v235, 3, v200
	v_lshl_add_u32 v213, v214, 4, v213
	ds_write_b64 v226, v[66:67] offset:6656
	v_cvt_pk_bf16_f32 v66, v182, v183
	v_cvt_pk_bf16_f32 v67, v184, v185
	v_cvt_pk_bf16_f32 v70, v70, v71
	v_cvt_pk_bf16_f32 v71, v72, v73
	ds_write_b64 v212, v[70:71]
	ds_write_b64 v225, v[66:67] offset:7168
	v_cvt_pk_bf16_f32 v66, v178, v179
	v_cvt_pk_bf16_f32 v67, v180, v181
	ds_write_b64 v224, v[66:67] offset:7680
	v_lshl_or_b32 v66, v200, 13, v198
	ds_read_b128 v[66:69], v66
	v_lshlrev_b32_e32 v220, 11, v200
	v_or_b32_e32 v70, v204, v220
	ds_read_b128 v[70:73], v70
	ds_read_b128 v[74:77], v223
	v_lshlrev_b32_e32 v232, 3, v200
	v_or_b32_e32 v214, 1, v232
	s_waitcnt lgkmcnt(0)
	v_mfma_f32_16x16x32_bf16 v[70:73], v[70:73], v[74:77], 0
	v_lshlrev_b32_e32 v215, 8, v214
	v_or_b32_e32 v78, v204, v215
	v_or_b32_e32 v184, 2, v232
	v_mfma_f32_16x16x32_bf16 v[66:69], v[66:69], v[74:77], 0
	v_lshl_or_b32 v74, v214, 10, v198
	ds_read_b128 v[74:77], v74
	ds_read_b128 v[78:81], v78
	ds_read_b128 v[82:85], v222
	v_lshlrev_b32_e32 v185, 8, v184
	s_waitcnt lgkmcnt(0)
	v_mfma_f32_16x16x32_bf16 v[70:73], v[78:81], v[82:85], v[70:73]
	v_or_b32_e32 v78, v204, v185
	v_or_b32_e32 v182, 3, v232
	v_lshlrev_b32_e32 v183, 8, v182
	v_mfma_f32_16x16x32_bf16 v[66:69], v[74:77], v[82:85], v[66:69]
	v_lshl_or_b32 v74, v184, 10, v198
	ds_read_b128 v[74:77], v74
	ds_read_b128 v[78:81], v78
	ds_read_b128 v[82:85], v221
	s_waitcnt lgkmcnt(0)
	v_mfma_f32_16x16x32_bf16 v[70:73], v[78:81], v[82:85], v[70:73]
	v_or_b32_e32 v78, v204, v183
	v_or_b32_e32 v180, 4, v232
	v_lshlrev_b32_e32 v181, 8, v180
	v_mfma_f32_16x16x32_bf16 v[66:69], v[74:77], v[82:85], v[66:69]
	v_lshl_or_b32 v74, v182, 10, v198
	ds_read_b128 v[74:77], v74
	ds_read_b128 v[78:81], v78
	ds_read_b128 v[82:85], v219
	s_waitcnt lgkmcnt(0)
	v_mfma_f32_16x16x32_bf16 v[66:69], v[74:77], v[82:85], v[66:69]
	v_lshl_or_b32 v74, v180, 10, v198
	ds_read_b128 v[74:77], v74
	v_or_b32_e32 v178, 5, v232
	v_mfma_f32_16x16x32_bf16 v[70:73], v[78:81], v[82:85], v[70:73]
	v_or_b32_e32 v78, v204, v181
	ds_read_b128 v[78:81], v78
	ds_read_b128 v[82:85], v218
	v_lshlrev_b32_e32 v179, 8, v178
	s_waitcnt lgkmcnt(0)
	v_mfma_f32_16x16x32_bf16 v[66:69], v[74:77], v[82:85], v[66:69]
	v_lshl_or_b32 v74, v178, 10, v198
	ds_read_b128 v[74:77], v74
	v_or_b32_e32 v176, 6, v232
	v_mfma_f32_16x16x32_bf16 v[70:73], v[78:81], v[82:85], v[70:73]
	v_or_b32_e32 v78, v204, v179
	ds_read_b128 v[78:81], v78
	ds_read_b128 v[82:85], v217
	v_lshlrev_b32_e32 v177, 8, v176
	s_waitcnt lgkmcnt(0)
	v_mfma_f32_16x16x32_bf16 v[66:69], v[74:77], v[82:85], v[66:69]
	v_lshl_or_b32 v74, v176, 10, v198
	ds_read_b128 v[74:77], v74
	v_or_b32_e32 v174, 7, v232
	v_mfma_f32_16x16x32_bf16 v[70:73], v[78:81], v[82:85], v[70:73]
	v_or_b32_e32 v78, v204, v177
	ds_read_b128 v[78:81], v78
	ds_read_b128 v[82:85], v216
	v_lshlrev_b32_e32 v175, 8, v174
	s_waitcnt lgkmcnt(0)
	v_mfma_f32_16x16x32_bf16 v[66:69], v[74:77], v[82:85], v[66:69]
	v_lshl_or_b32 v74, v174, 10, v198
	s_waitcnt vmcnt(16)
	v_cvt_pk_bf16_f32 v14, v14, v15
	v_cvt_pk_bf16_f32 v15, v16, v17
	v_mfma_f32_16x16x32_bf16 v[70:73], v[78:81], v[82:85], v[70:73]
	v_or_b32_e32 v78, v204, v175
	ds_read_b128 v[74:77], v74
	ds_read_b128 v[78:81], v78
	ds_read_b128 v[82:85], v213
	ds_write_b64 v209, v[14:15] offset:1536
	v_cvt_pk_bf16_f32 v14, v46, v47
	v_cvt_pk_bf16_f32 v15, v48, v49
	ds_write_b64 v208, v[14:15] offset:2048
	v_cvt_pk_bf16_f32 v14, v18, v19
	v_cvt_pk_bf16_f32 v15, v20, v21
	ds_write_b64 v207, v[14:15] offset:2560
	v_cvt_pk_bf16_f32 v14, v50, v51
	v_cvt_pk_bf16_f32 v15, v52, v53
	ds_write_b64 v206, v[14:15] offset:3072
	v_cvt_pk_bf16_f32 v14, v22, v23
	v_cvt_pk_bf16_f32 v15, v24, v25
	ds_write_b64 v205, v[14:15] offset:3584
	v_cvt_pk_bf16_f32 v14, v54, v55
	v_cvt_pk_bf16_f32 v15, v56, v57
	v_cvt_pk_bf16_f32 v6, v6, v7
	v_cvt_pk_bf16_f32 v2, v2, v3
	ds_write_b64 v231, v[14:15] offset:4096
	v_cvt_pk_bf16_f32 v14, v26, v27
	v_cvt_pk_bf16_f32 v15, v28, v29
	v_cvt_pk_bf16_f32 v7, v8, v9
	ds_write_b64 v226, v[6:7] offset:6656
	v_cvt_pk_bf16_f32 v6, v10, v11
	v_cvt_pk_bf16_f32 v3, v4, v5
	ds_write_b64 v224, v[2:3] offset:7680
	v_lshlrev_b32_e32 v2, 10, v235
	ds_write_b64 v230, v[14:15] offset:4608
	v_cvt_pk_bf16_f32 v14, v58, v59
	v_cvt_pk_bf16_f32 v15, v60, v61
	v_cvt_pk_bf16_f32 v7, v12, v13
	ds_write_b64 v225, v[6:7] offset:7168
	v_and_or_b32 v6, v2, s0, v203
	ds_write_b64 v229, v[14:15] offset:5120
	v_cvt_pk_bf16_f32 v14, v30, v31
	v_cvt_pk_bf16_f32 v15, v32, v33
	v_or_b32_e32 v7, 0x2000, v6
	ds_write_b64 v228, v[14:15] offset:5632
	v_cvt_pk_bf16_f32 v14, v34, v35
	v_cvt_pk_bf16_f32 v15, v36, v37
	buffer_load_dwordx4 v[2:5], v6, s[4:7], 0 offen nt
	buffer_load_dwordx4 v[10:13], v7, s[4:7], 0 offen nt
	v_or_b32_e32 v7, 0x4000, v6
	ds_write_b64 v227, v[14:15] offset:6144
	buffer_load_dwordx4 v[14:17], v7, s[4:7], 0 offen nt
	v_or_b32_e32 v7, 0x6000, v6
	v_cvt_pk_bf16_f32 v38, v38, v39
	v_cvt_pk_bf16_f32 v39, v40, v41
	buffer_load_dwordx4 v[22:25], v7, s[4:7], 0 offen nt
	v_or_b32_e32 v7, 0x8000, v6
	ds_write_b64 v211, v[38:39] offset:512
	v_cvt_pk_bf16_f32 v38, v42, v43
	v_cvt_pk_bf16_f32 v39, v44, v45
	buffer_load_dwordx4 v[30:33], v7, s[4:7], 0 offen nt
	v_or_b32_e32 v7, 0xa000, v6
	ds_write_b64 v210, v[38:39] offset:1024
	buffer_load_dwordx4 v[38:41], v7, s[4:7], 0 offen nt
	v_or_b32_e32 v7, 0xc000, v6
	buffer_load_dwordx4 v[46:49], v7, s[4:7], 0 offen nt
	v_or_b32_e32 v7, 0xe000, v6
	v_cvt_pk_bf16_f32 v62, v62, v63
	v_cvt_pk_bf16_f32 v63, v64, v65
	buffer_load_dwordx4 v[54:57], v7, s[4:7], 0 offen nt
	v_or_b32_e32 v7, 0x10000, v6
	ds_write_b64 v212, v[62:63]
	buffer_load_dwordx4 v[62:65], v7, s[4:7], 0 offen nt
	v_or_b32_e32 v7, 0x12000, v6
	s_waitcnt lgkmcnt(14)
	v_mfma_f32_16x16x32_bf16 v[66:69], v[74:77], v[82:85], v[66:69]
	v_mfma_f32_16x16x32_bf16 v[74:77], v[78:81], v[82:85], v[70:73]
	s_nop 2
	buffer_load_dwordx4 v[70:73], v7, s[4:7], 0 offen nt
	v_or_b32_e32 v7, 0x14000, v6
	buffer_load_dwordx4 v[78:81], v7, s[4:7], 0 offen nt
	v_or_b32_e32 v7, 0x16000, v6
	buffer_load_dwordx4 v[86:89], v7, s[4:7], 0 offen nt
	v_or_b32_e32 v7, 0x18000, v6
	buffer_load_dwordx4 v[94:97], v7, s[4:7], 0 offen nt
	v_or_b32_e32 v7, 0x1a000, v6
	buffer_load_dwordx4 v[146:149], v7, s[4:7], 0 offen nt
	v_or_b32_e32 v7, 0x1c000, v6
	v_or_b32_e32 v6, 0x1e000, v6
	buffer_load_dwordx4 v[150:153], v7, s[4:7], 0 offen nt
	buffer_load_dwordx4 v[154:157], v6, s[4:7], 0 offen nt
	v_add_u32_e32 v6, 8, v232
	v_and_b32_e32 v50, 56, v6
	v_lshl_or_b32 v6, v50, 10, v198
	ds_read_b128 v[6:9], v6
	v_lshl_or_b32 v18, v50, 8, v204
	ds_read_b128 v[18:21], v18
	ds_read_b128 v[26:29], v223
	v_or_b32_e32 v34, 1, v50
	s_movk_i32 s24, 0x1000
	s_waitcnt lgkmcnt(0)
	v_mfma_f32_16x16x32_bf16 v[18:21], v[18:21], v[26:29], v[74:77]
	v_add_u32_e32 v234, 5, v200
	v_mfma_f32_16x16x32_bf16 v[6:9], v[6:9], v[26:29], v[66:69]
	v_lshl_or_b32 v26, v34, 10, v198
	ds_read_b128 v[26:29], v26
	v_lshl_or_b32 v34, v34, 8, v204
	ds_read_b128 v[34:37], v34
	ds_read_b128 v[42:45], v222
	s_waitcnt lgkmcnt(0)
	v_mfma_f32_16x16x32_bf16 v[18:21], v[34:37], v[42:45], v[18:21]
	v_or_b32_e32 v34, 2, v50
	v_mfma_f32_16x16x32_bf16 v[6:9], v[26:29], v[42:45], v[6:9]
	v_lshl_or_b32 v26, v34, 10, v198
	ds_read_b128 v[26:29], v26
	v_lshl_or_b32 v34, v34, 8, v204
	ds_read_b128 v[34:37], v34
	ds_read_b128 v[42:45], v221
	s_waitcnt lgkmcnt(0)
	v_mfma_f32_16x16x32_bf16 v[18:21], v[34:37], v[42:45], v[18:21]
	v_or_b32_e32 v34, 3, v50
	v_mfma_f32_16x16x32_bf16 v[6:9], v[26:29], v[42:45], v[6:9]
	v_lshl_or_b32 v26, v34, 10, v198
	ds_read_b128 v[26:29], v26
	v_lshl_or_b32 v34, v34, 8, v204
	ds_read_b128 v[34:37], v34
	ds_read_b128 v[42:45], v219
	s_waitcnt lgkmcnt(0)
	v_mfma_f32_16x16x32_bf16 v[18:21], v[34:37], v[42:45], v[18:21]
	v_or_b32_e32 v34, 4, v50
	v_mfma_f32_16x16x32_bf16 v[6:9], v[26:29], v[42:45], v[6:9]
	v_lshl_or_b32 v26, v34, 10, v198
	ds_read_b128 v[26:29], v26
	v_lshl_or_b32 v34, v34, 8, v204
	ds_read_b128 v[34:37], v34
	ds_read_b128 v[42:45], v218
	s_waitcnt lgkmcnt(0)
	v_mfma_f32_16x16x32_bf16 v[18:21], v[34:37], v[42:45], v[18:21]
	v_or_b32_e32 v34, 5, v50
	v_mfma_f32_16x16x32_bf16 v[6:9], v[26:29], v[42:45], v[6:9]
	v_lshl_or_b32 v26, v34, 10, v198
	ds_read_b128 v[26:29], v26
	v_lshl_or_b32 v34, v34, 8, v204
	ds_read_b128 v[34:37], v34
	ds_read_b128 v[42:45], v217
	s_waitcnt lgkmcnt(0)
	v_mfma_f32_16x16x32_bf16 v[18:21], v[34:37], v[42:45], v[18:21]
	v_or_b32_e32 v34, 6, v50
	v_mfma_f32_16x16x32_bf16 v[6:9], v[26:29], v[42:45], v[6:9]
	v_lshl_or_b32 v26, v34, 10, v198
	ds_read_b128 v[26:29], v26
	v_lshl_or_b32 v34, v34, 8, v204
	ds_read_b128 v[34:37], v34
	ds_read_b128 v[42:45], v216
	s_waitcnt lgkmcnt(0)
	v_mfma_f32_16x16x32_bf16 v[18:21], v[34:37], v[42:45], v[18:21]
	v_or_b32_e32 v34, 7, v50
	v_mfma_f32_16x16x32_bf16 v[6:9], v[26:29], v[42:45], v[6:9]
	v_lshl_or_b32 v26, v34, 10, v198
	ds_read_b128 v[26:29], v26
	v_lshl_or_b32 v34, v34, 8, v204
	ds_read_b128 v[34:37], v34
	ds_read_b128 v[42:45], v213
	s_waitcnt lgkmcnt(0)
	v_mfma_f32_16x16x32_bf16 v[162:165], v[26:29], v[42:45], v[6:9]
	s_waitcnt vmcnt(31)
	s_nop 1
	v_cvt_pk_bf16_f32 v6, v102, v103
	v_cvt_pk_bf16_f32 v7, v104, v105
	ds_write_b64 v212, v[6:7]
	s_waitcnt vmcnt(30)
	v_cvt_pk_bf16_f32 v6, v98, v99
	v_cvt_pk_bf16_f32 v7, v100, v101
	ds_write_b64 v211, v[6:7] offset:512
	s_waitcnt vmcnt(29)
	v_cvt_pk_bf16_f32 v6, v110, v111
	v_cvt_pk_bf16_f32 v7, v112, v113
	ds_write_b64 v210, v[6:7] offset:1024
	s_waitcnt vmcnt(28)
	v_cvt_pk_bf16_f32 v6, v106, v107
	v_cvt_pk_bf16_f32 v7, v108, v109
	ds_write_b64 v209, v[6:7] offset:1536
	s_waitcnt vmcnt(27)
	v_cvt_pk_bf16_f32 v6, v118, v119
	v_cvt_pk_bf16_f32 v7, v120, v121
	ds_write_b64 v208, v[6:7] offset:2048
	s_waitcnt vmcnt(26)
	v_cvt_pk_bf16_f32 v6, v114, v115
	v_cvt_pk_bf16_f32 v7, v116, v117
	ds_write_b64 v207, v[6:7] offset:2560
	s_waitcnt vmcnt(25)
	v_cvt_pk_bf16_f32 v6, v126, v127
	v_cvt_pk_bf16_f32 v7, v128, v129
	ds_write_b64 v206, v[6:7] offset:3072
	s_waitcnt vmcnt(24)
	v_cvt_pk_bf16_f32 v6, v122, v123
	v_cvt_pk_bf16_f32 v7, v124, v125
	ds_write_b64 v205, v[6:7] offset:3584
	s_waitcnt vmcnt(23)
	v_cvt_pk_bf16_f32 v6, v134, v135
	v_cvt_pk_bf16_f32 v7, v136, v137
	ds_write_b64 v231, v[6:7] offset:4096
	s_waitcnt vmcnt(22)
	v_cvt_pk_bf16_f32 v6, v130, v131
	v_cvt_pk_bf16_f32 v7, v132, v133
	ds_write_b64 v230, v[6:7] offset:4608
	s_waitcnt vmcnt(21)
	v_cvt_pk_bf16_f32 v6, v142, v143
	v_cvt_pk_bf16_f32 v7, v144, v145
	ds_write_b64 v229, v[6:7] offset:5120
	s_waitcnt vmcnt(20)
	v_cvt_pk_bf16_f32 v6, v138, v139
	v_cvt_pk_bf16_f32 v7, v140, v141
	ds_write_b64 v228, v[6:7] offset:5632
	s_waitcnt vmcnt(19)
	v_cvt_pk_bf16_f32 v6, v170, v171
	v_cvt_pk_bf16_f32 v7, v172, v173
	ds_write_b64 v227, v[6:7] offset:6144
	s_waitcnt vmcnt(18)
	v_cvt_pk_bf16_f32 v6, v158, v159
	v_mov_b32_e32 v106, 0x1000
	v_cvt_pk_bf16_f32 v7, v160, v161
	ds_write_b64 v226, v[6:7] offset:6656
	s_waitcnt vmcnt(17)
	v_cvt_pk_bf16_f32 v6, v190, v191
	v_bitop3_b32 v107, v233, s19, v106 bitop3:0xde
	v_mfma_f32_16x16x32_bf16 v[166:169], v[34:37], v[42:45], v[18:21]
	v_cvt_pk_bf16_f32 v7, v192, v193
	ds_write_b64 v225, v[6:7] offset:7168
	s_waitcnt vmcnt(16)
	v_cvt_pk_bf16_f32 v6, v186, v187
	v_bitop3_b32 v26, v233, s17, v106 bitop3:0xde
	v_bitop3_b32 v34, v233, s11, v106 bitop3:0xde
	v_bitop3_b32 v18, v233, s16, v106 bitop3:0xde
	v_bitop3_b32 v42, v233, s13, v106 bitop3:0xde
	v_bitop3_b32 v50, v233, s10, v106 bitop3:0xde
	v_bitop3_b32 v58, v233, s12, v106 bitop3:0xde
	v_bitop3_b32 v66, v233, s1, v106 bitop3:0xde
	v_bitop3_b32 v74, v233, s18, v106 bitop3:0xde
	v_bitop3_b32 v82, v233, s23, v106 bitop3:0xde
	v_bitop3_b32 v90, v233, s22, v106 bitop3:0xde
	v_bitop3_b32 v98, v233, s21, v106 bitop3:0xde
	v_bitop3_b32 v102, v233, s20, v106 bitop3:0xde
	buffer_load_dwordx4 v[110:113], v107, s[4:7], 0 offen nt
	v_bitop3_b32 v107, v233, s15, v106 bitop3:0xde
	v_bitop3_b32 v106, v233, s14, v106 bitop3:0xde
	v_cvt_pk_bf16_f32 v7, v188, v189
	ds_write_b64 v224, v[6:7] offset:7680
	v_bitop3_b32 v6, v203, s24, v196 bitop3:0x36
	buffer_load_dwordx4 v[42:45], v42, s[4:7], 0 offen nt
	s_nop 0
	buffer_load_dwordx4 v[50:53], v50, s[4:7], 0 offen nt
	s_nop 0
	buffer_load_dwordx4 v[58:61], v58, s[4:7], 0 offen nt
	s_nop 0
	buffer_load_dwordx4 v[66:69], v66, s[4:7], 0 offen nt
	s_nop 0
	buffer_load_dwordx4 v[74:77], v74, s[4:7], 0 offen nt
	s_nop 0
	buffer_load_dwordx4 v[82:85], v82, s[4:7], 0 offen nt
	s_nop 0
	buffer_load_dwordx4 v[90:93], v90, s[4:7], 0 offen nt
	s_nop 0
	buffer_load_dwordx4 v[98:101], v98, s[4:7], 0 offen nt
	s_nop 0
	buffer_load_dwordx4 v[102:105], v102, s[4:7], 0 offen nt
	s_nop 0
	buffer_load_dwordx4 v[126:129], v106, s[4:7], 0 offen nt
	buffer_load_dwordx4 v[118:121], v107, s[4:7], 0 offen nt
	s_nop 0
	buffer_load_dwordx4 v[6:9], v6, s[4:7], 0 offen nt
	s_nop 0
	buffer_load_dwordx4 v[18:21], v18, s[4:7], 0 offen nt
	s_nop 0
	buffer_load_dwordx4 v[26:29], v26, s[4:7], 0 offen nt
	s_nop 0
	buffer_load_dwordx4 v[34:37], v34, s[4:7], 0 offen nt
	v_add_u32_e32 v106, 16, v232
	v_and_b32_e32 v138, 56, v106
	v_lshl_or_b32 v106, v138, 10, v198
	ds_read_b128 v[106:109], v106
	v_lshl_or_b32 v114, v138, 8, v204
	ds_read_b128 v[114:117], v114
	ds_read_b128 v[122:125], v223
	v_or_b32_e32 v130, 1, v138
	s_waitcnt vmcnt(31)
	v_cvt_pk_bf16_f32 v2, v2, v3
	s_waitcnt lgkmcnt(0)
	v_mfma_f32_16x16x32_bf16 v[114:117], v[114:117], v[122:125], v[166:169]
	v_cvt_pk_bf16_f32 v3, v4, v5
	v_mfma_f32_16x16x32_bf16 v[106:109], v[106:109], v[122:125], v[162:165]
	v_lshl_or_b32 v122, v130, 10, v198
	ds_read_b128 v[122:125], v122
	v_lshl_or_b32 v130, v130, 8, v204
	ds_read_b128 v[130:133], v130
	ds_read_b128 v[134:137], v222
	s_waitcnt lgkmcnt(0)
	v_mfma_f32_16x16x32_bf16 v[114:117], v[130:133], v[134:137], v[114:117]
	v_or_b32_e32 v130, 2, v138
	v_mfma_f32_16x16x32_bf16 v[106:109], v[122:125], v[134:137], v[106:109]
	v_lshl_or_b32 v122, v130, 10, v198
	ds_read_b128 v[122:125], v122
	v_lshl_or_b32 v130, v130, 8, v204
	ds_read_b128 v[130:133], v130
	ds_read_b128 v[134:137], v221
	s_waitcnt lgkmcnt(0)
	v_mfma_f32_16x16x32_bf16 v[114:117], v[130:133], v[134:137], v[114:117]
	v_or_b32_e32 v130, 3, v138
	v_mfma_f32_16x16x32_bf16 v[106:109], v[122:125], v[134:137], v[106:109]
	v_lshl_or_b32 v122, v130, 10, v198
	ds_read_b128 v[122:125], v122
	v_lshl_or_b32 v130, v130, 8, v204
	ds_read_b128 v[130:133], v130
	ds_read_b128 v[134:137], v219
	s_waitcnt lgkmcnt(0)
	v_mfma_f32_16x16x32_bf16 v[114:117], v[130:133], v[134:137], v[114:117]
	v_or_b32_e32 v130, 4, v138
	v_mfma_f32_16x16x32_bf16 v[106:109], v[122:125], v[134:137], v[106:109]
	v_lshl_or_b32 v122, v130, 10, v198
	ds_read_b128 v[122:125], v122
	v_lshl_or_b32 v130, v130, 8, v204
	ds_read_b128 v[130:133], v130
	ds_read_b128 v[134:137], v218
	s_waitcnt lgkmcnt(0)
	v_mfma_f32_16x16x32_bf16 v[114:117], v[130:133], v[134:137], v[114:117]
	v_or_b32_e32 v130, 5, v138
	v_mfma_f32_16x16x32_bf16 v[106:109], v[122:125], v[134:137], v[106:109]
	v_lshl_or_b32 v122, v130, 10, v198
	ds_read_b128 v[122:125], v122
	v_lshl_or_b32 v130, v130, 8, v204
	ds_read_b128 v[130:133], v130
	ds_read_b128 v[134:137], v217
	s_waitcnt lgkmcnt(0)
	v_mfma_f32_16x16x32_bf16 v[114:117], v[130:133], v[134:137], v[114:117]
	v_or_b32_e32 v130, 6, v138
	v_mfma_f32_16x16x32_bf16 v[106:109], v[122:125], v[134:137], v[106:109]
	v_lshl_or_b32 v122, v130, 10, v198
	ds_read_b128 v[122:125], v122
	v_lshl_or_b32 v130, v130, 8, v204
	ds_read_b128 v[130:133], v130
	ds_read_b128 v[134:137], v216
	s_waitcnt lgkmcnt(0)
	v_mfma_f32_16x16x32_bf16 v[114:117], v[130:133], v[134:137], v[114:117]
	v_or_b32_e32 v130, 7, v138
	v_mfma_f32_16x16x32_bf16 v[106:109], v[122:125], v[134:137], v[106:109]
	v_lshl_or_b32 v122, v130, 10, v198
	v_lshl_or_b32 v130, v130, 8, v204
	ds_read_b128 v[122:125], v122
	ds_read_b128 v[134:137], v130
	ds_read_b128 v[138:141], v213
	ds_write_b64 v212, v[2:3]
	s_waitcnt vmcnt(30)
	v_cvt_pk_bf16_f32 v2, v10, v11
	v_cvt_pk_bf16_f32 v3, v12, v13
	ds_write_b64 v211, v[2:3] offset:512
	s_waitcnt vmcnt(29)
	v_cvt_pk_bf16_f32 v2, v14, v15
	v_cvt_pk_bf16_f32 v3, v16, v17
	ds_write_b64 v210, v[2:3] offset:1024
	s_waitcnt vmcnt(28)
	v_cvt_pk_bf16_f32 v2, v22, v23
	v_cvt_pk_bf16_f32 v3, v24, v25
	ds_write_b64 v209, v[2:3] offset:1536
	s_waitcnt vmcnt(27)
	v_cvt_pk_bf16_f32 v2, v30, v31
	v_cvt_pk_bf16_f32 v3, v32, v33
	ds_write_b64 v208, v[2:3] offset:2048
	s_waitcnt vmcnt(26)
	v_cvt_pk_bf16_f32 v2, v38, v39
	v_cvt_pk_bf16_f32 v3, v40, v41
	ds_write_b64 v207, v[2:3] offset:2560
	s_waitcnt vmcnt(25)
	v_cvt_pk_bf16_f32 v2, v46, v47
	v_cvt_pk_bf16_f32 v3, v48, v49
	ds_write_b64 v206, v[2:3] offset:3072
	s_waitcnt vmcnt(24)
	v_cvt_pk_bf16_f32 v2, v54, v55
	v_cvt_pk_bf16_f32 v3, v56, v57
	ds_write_b64 v205, v[2:3] offset:3584
	s_waitcnt vmcnt(23)
	v_cvt_pk_bf16_f32 v2, v62, v63
	v_cvt_pk_bf16_f32 v3, v64, v65
	ds_write_b64 v231, v[2:3] offset:4096
	s_waitcnt vmcnt(22)
	v_cvt_pk_bf16_f32 v2, v70, v71
	v_cvt_pk_bf16_f32 v3, v72, v73
	ds_write_b64 v230, v[2:3] offset:4608
	s_waitcnt vmcnt(21)
	v_cvt_pk_bf16_f32 v2, v78, v79
	v_cvt_pk_bf16_f32 v3, v80, v81
	ds_write_b64 v229, v[2:3] offset:5120
	s_waitcnt vmcnt(20)
	v_cvt_pk_bf16_f32 v2, v86, v87
	v_cvt_pk_bf16_f32 v3, v88, v89
	ds_write_b64 v228, v[2:3] offset:5632
	s_waitcnt vmcnt(19)
	v_cvt_pk_bf16_f32 v2, v94, v95
	v_cvt_pk_bf16_f32 v3, v96, v97
	ds_write_b64 v227, v[2:3] offset:6144
	s_waitcnt vmcnt(18)
	v_cvt_pk_bf16_f32 v2, v146, v147
	v_cvt_pk_bf16_f32 v3, v148, v149
	ds_write_b64 v226, v[2:3] offset:6656
	s_waitcnt vmcnt(17)
	v_cvt_pk_bf16_f32 v2, v150, v151
	v_cvt_pk_bf16_f32 v3, v152, v153
	ds_write_b64 v225, v[2:3] offset:7168
	s_waitcnt vmcnt(16)
	v_cvt_pk_bf16_f32 v2, v154, v155
	v_cvt_pk_bf16_f32 v3, v156, v157
	ds_write_b64 v224, v[2:3] offset:7680
	v_lshlrev_b32_e32 v2, 10, v234
	s_waitcnt lgkmcnt(14)
	v_mfma_f32_16x16x32_bf16 v[130:133], v[122:125], v[138:141], v[106:109]
	v_and_or_b32 v122, v2, s0, v203
	buffer_load_dwordx4 v[2:5], v122, s[4:7], 0 offen nt
	v_or_b32_e32 v10, 0x2000, v122
	v_mfma_f32_16x16x32_bf16 v[134:137], v[134:137], v[138:141], v[114:117]
	v_or_b32_e32 v14, 0x4000, v122
	v_or_b32_e32 v22, 0x6000, v122
	v_or_b32_e32 v30, 0x8000, v122
	v_or_b32_e32 v38, 0xa000, v122
	v_or_b32_e32 v46, 0xc000, v122
	v_or_b32_e32 v54, 0xe000, v122
	v_or_b32_e32 v62, 0x10000, v122
	v_or_b32_e32 v70, 0x12000, v122
	v_or_b32_e32 v78, 0x14000, v122
	v_or_b32_e32 v86, 0x16000, v122
	v_or_b32_e32 v94, 0x18000, v122
	v_or_b32_e32 v106, 0x1a000, v122
	v_or_b32_e32 v114, 0x1c000, v122
	v_or_b32_e32 v122, 0x1e000, v122
	buffer_load_dwordx4 v[54:57], v54, s[4:7], 0 offen nt
	s_nop 0
	buffer_load_dwordx4 v[62:65], v62, s[4:7], 0 offen nt
	s_nop 0
	buffer_load_dwordx4 v[70:73], v70, s[4:7], 0 offen nt
	s_nop 0
	buffer_load_dwordx4 v[78:81], v78, s[4:7], 0 offen nt
	s_nop 0
	buffer_load_dwordx4 v[86:89], v86, s[4:7], 0 offen nt
	s_nop 0
	buffer_load_dwordx4 v[94:97], v94, s[4:7], 0 offen nt
	s_nop 0
	buffer_load_dwordx4 v[106:109], v106, s[4:7], 0 offen nt
	s_nop 0
	buffer_load_dwordx4 v[114:117], v114, s[4:7], 0 offen nt
	s_nop 0
	buffer_load_dwordx4 v[122:125], v122, s[4:7], 0 offen nt
	s_nop 0
	buffer_load_dwordx4 v[10:13], v10, s[4:7], 0 offen nt
	s_nop 0
	buffer_load_dwordx4 v[14:17], v14, s[4:7], 0 offen nt
	s_nop 0
	buffer_load_dwordx4 v[22:25], v22, s[4:7], 0 offen nt
	s_nop 0
	buffer_load_dwordx4 v[30:33], v30, s[4:7], 0 offen nt
	s_nop 0
	buffer_load_dwordx4 v[38:41], v38, s[4:7], 0 offen nt
	s_nop 0
	buffer_load_dwordx4 v[46:49], v46, s[4:7], 0 offen nt
	v_lshlrev_b32_e32 v138, 3, v235
	v_and_b32_e32 v150, 56, v138
	v_lshl_or_b32 v138, v150, 10, v198
	ds_read_b128 v[138:141], v138
	v_lshl_or_b32 v142, v150, 8, v204
	ds_read_b128 v[142:145], v142
	ds_read_b128 v[146:149], v223
	s_waitcnt vmcnt(19)
	v_cvt_pk_bf16_f32 v6, v6, v7
	v_cvt_pk_bf16_f32 v7, v8, v9
	s_waitcnt lgkmcnt(0)
	v_mfma_f32_16x16x32_bf16 v[134:137], v[142:145], v[146:149], v[134:137]
	v_or_b32_e32 v142, 1, v150
	v_mfma_f32_16x16x32_bf16 v[130:133], v[138:141], v[146:149], v[130:133]
	v_lshl_or_b32 v138, v142, 10, v198
	ds_read_b128 v[138:141], v138
	v_lshl_or_b32 v142, v142, 8, v204
	ds_read_b128 v[142:145], v142
	ds_read_b128 v[146:149], v222
	s_waitcnt lgkmcnt(0)
	v_mfma_f32_16x16x32_bf16 v[134:137], v[142:145], v[146:149], v[134:137]
	v_or_b32_e32 v142, 2, v150
	v_mfma_f32_16x16x32_bf16 v[130:133], v[138:141], v[146:149], v[130:133]
	v_lshl_or_b32 v138, v142, 10, v198
	ds_read_b128 v[138:141], v138
	v_lshl_or_b32 v142, v142, 8, v204
	ds_read_b128 v[142:145], v142
	ds_read_b128 v[146:149], v221
	s_waitcnt lgkmcnt(0)
	v_mfma_f32_16x16x32_bf16 v[134:137], v[142:145], v[146:149], v[134:137]
	v_or_b32_e32 v142, 3, v150
	v_mfma_f32_16x16x32_bf16 v[130:133], v[138:141], v[146:149], v[130:133]
	v_lshl_or_b32 v138, v142, 10, v198
	ds_read_b128 v[138:141], v138
	v_lshl_or_b32 v142, v142, 8, v204
	ds_read_b128 v[142:145], v142
	ds_read_b128 v[146:149], v219
	s_waitcnt lgkmcnt(0)
	v_mfma_f32_16x16x32_bf16 v[134:137], v[142:145], v[146:149], v[134:137]
	v_or_b32_e32 v142, 4, v150
	v_mfma_f32_16x16x32_bf16 v[130:133], v[138:141], v[146:149], v[130:133]
	v_lshl_or_b32 v138, v142, 10, v198
	ds_read_b128 v[138:141], v138
	v_lshl_or_b32 v142, v142, 8, v204
	ds_read_b128 v[142:145], v142
	ds_read_b128 v[146:149], v218
	s_waitcnt lgkmcnt(0)
	v_mfma_f32_16x16x32_bf16 v[134:137], v[142:145], v[146:149], v[134:137]
	v_or_b32_e32 v142, 5, v150
	v_mfma_f32_16x16x32_bf16 v[130:133], v[138:141], v[146:149], v[130:133]
	v_lshl_or_b32 v138, v142, 10, v198
	ds_read_b128 v[138:141], v138
	v_lshl_or_b32 v142, v142, 8, v204
	ds_read_b128 v[142:145], v142
	ds_read_b128 v[146:149], v217
	s_waitcnt lgkmcnt(0)
	v_mfma_f32_16x16x32_bf16 v[134:137], v[142:145], v[146:149], v[134:137]
	v_or_b32_e32 v142, 6, v150
	v_mfma_f32_16x16x32_bf16 v[130:133], v[138:141], v[146:149], v[130:133]
	v_lshl_or_b32 v138, v142, 10, v198
	ds_read_b128 v[138:141], v138
	v_lshl_or_b32 v142, v142, 8, v204
	ds_read_b128 v[142:145], v142
	ds_read_b128 v[146:149], v216
	s_waitcnt lgkmcnt(0)
	v_mfma_f32_16x16x32_bf16 v[134:137], v[142:145], v[146:149], v[134:137]
	v_or_b32_e32 v142, 7, v150
	v_mfma_f32_16x16x32_bf16 v[130:133], v[138:141], v[146:149], v[130:133]
	v_lshl_or_b32 v138, v142, 10, v198
	v_lshl_or_b32 v142, v142, 8, v204
	ds_read_b128 v[138:141], v138
	ds_read_b128 v[142:145], v142
	ds_read_b128 v[146:149], v213
	ds_write_b64 v212, v[6:7]
	s_waitcnt vmcnt(18)
	v_cvt_pk_bf16_f32 v6, v18, v19
	v_cvt_pk_bf16_f32 v7, v20, v21
	ds_write_b64 v211, v[6:7] offset:512
	s_waitcnt vmcnt(17)
	v_cvt_pk_bf16_f32 v6, v26, v27
	v_cvt_pk_bf16_f32 v7, v28, v29
	ds_write_b64 v210, v[6:7] offset:1024
	s_waitcnt vmcnt(16)
	v_cvt_pk_bf16_f32 v6, v34, v35
	v_cvt_pk_bf16_f32 v7, v36, v37
	ds_write_b64 v209, v[6:7] offset:1536
	v_cvt_pk_bf16_f32 v6, v42, v43
	v_cvt_pk_bf16_f32 v7, v44, v45
	ds_write_b64 v208, v[6:7] offset:2048
	v_cvt_pk_bf16_f32 v6, v50, v51
	v_cvt_pk_bf16_f32 v7, v52, v53
	ds_write_b64 v207, v[6:7] offset:2560
	v_cvt_pk_bf16_f32 v6, v58, v59
	v_cvt_pk_bf16_f32 v7, v60, v61
	ds_write_b64 v206, v[6:7] offset:3072
	v_cvt_pk_bf16_f32 v6, v66, v67
	v_cvt_pk_bf16_f32 v7, v68, v69
	ds_write_b64 v205, v[6:7] offset:3584
	v_cvt_pk_bf16_f32 v6, v74, v75
	v_cvt_pk_bf16_f32 v7, v76, v77
	ds_write_b64 v231, v[6:7] offset:4096
	v_cvt_pk_bf16_f32 v6, v82, v83
	v_cvt_pk_bf16_f32 v7, v84, v85
	ds_write_b64 v230, v[6:7] offset:4608
	v_cvt_pk_bf16_f32 v6, v90, v91
	v_cvt_pk_bf16_f32 v7, v92, v93
	ds_write_b64 v229, v[6:7] offset:5120
	v_cvt_pk_bf16_f32 v6, v98, v99
	v_cvt_pk_bf16_f32 v7, v100, v101
	ds_write_b64 v228, v[6:7] offset:5632
	v_cvt_pk_bf16_f32 v6, v102, v103
	v_cvt_pk_bf16_f32 v7, v104, v105
	ds_write_b64 v227, v[6:7] offset:6144
	v_cvt_pk_bf16_f32 v6, v110, v111
	v_cvt_pk_bf16_f32 v7, v112, v113
	ds_write_b64 v226, v[6:7] offset:6656
	v_cvt_pk_bf16_f32 v6, v118, v119
	v_cvt_pk_bf16_f32 v7, v120, v121
	ds_write_b64 v225, v[6:7] offset:7168
	v_cvt_pk_bf16_f32 v6, v126, v127
	v_cvt_pk_bf16_f32 v7, v128, v129
	ds_write_b64 v224, v[6:7] offset:7680
	v_add_u32_e32 v6, 0x1800, v196
	v_and_or_b32 v126, v6, s0, v203
	buffer_load_dwordx4 v[6:9], v126, s[4:7], 0 offen nt
	v_or_b32_e32 v18, 0x2000, v126
	v_or_b32_e32 v26, 0x4000, v126
	v_or_b32_e32 v34, 0x6000, v126
	v_or_b32_e32 v42, 0x8000, v126
	v_or_b32_e32 v50, 0xa000, v126
	v_or_b32_e32 v58, 0xc000, v126
	v_or_b32_e32 v66, 0xe000, v126
	v_or_b32_e32 v74, 0x10000, v126
	v_or_b32_e32 v82, 0x12000, v126
	v_or_b32_e32 v90, 0x14000, v126
	v_or_b32_e32 v98, 0x16000, v126
	v_or_b32_e32 v102, 0x18000, v126
	v_or_b32_e32 v110, 0x1a000, v126
	v_or_b32_e32 v118, 0x1c000, v126
	v_or_b32_e32 v126, 0x1e000, v126
	buffer_load_dwordx4 v[50:53], v50, s[4:7], 0 offen nt
	s_waitcnt lgkmcnt(14)
	v_mfma_f32_16x16x32_bf16 v[130:133], v[138:141], v[146:149], v[130:133]
	buffer_load_dwordx4 v[58:61], v58, s[4:7], 0 offen nt
	s_nop 0
	buffer_load_dwordx4 v[66:69], v66, s[4:7], 0 offen nt
	v_mfma_f32_16x16x32_bf16 v[134:137], v[142:145], v[146:149], v[134:137]
	buffer_load_dwordx4 v[74:77], v74, s[4:7], 0 offen nt
	v_add_u32_e32 v142, 7, v200
	buffer_load_dwordx4 v[82:85], v82, s[4:7], 0 offen nt
	s_nop 0
	buffer_load_dwordx4 v[90:93], v90, s[4:7], 0 offen nt
	s_nop 0
	buffer_load_dwordx4 v[98:101], v98, s[4:7], 0 offen nt
	s_nop 0
	buffer_load_dwordx4 v[102:105], v102, s[4:7], 0 offen nt
	s_nop 0
	buffer_load_dwordx4 v[110:113], v110, s[4:7], 0 offen nt
	s_nop 0
	buffer_load_dwordx4 v[118:121], v118, s[4:7], 0 offen nt
	s_nop 0
	buffer_load_dwordx4 v[126:129], v126, s[4:7], 0 offen nt
	s_nop 0
	buffer_load_dwordx4 v[18:21], v18, s[4:7], 0 offen nt
	s_nop 0
	buffer_load_dwordx4 v[26:29], v26, s[4:7], 0 offen nt
	s_nop 0
	buffer_load_dwordx4 v[34:37], v34, s[4:7], 0 offen nt
	s_nop 0
	buffer_load_dwordx4 v[42:45], v42, s[4:7], 0 offen nt
	v_xor_b32_e32 v143, 32, v232
	v_lshl_or_b32 v138, v143, 10, v198
	ds_read_b128 v[138:141], v138
	v_lshl_or_b32 v143, v143, 8, v204
	ds_read_b128 v[144:147], v143
	ds_read_b128 v[148:151], v223
	v_bitop3_b32 v143, v232, 1, 32 bitop3:0xde
	s_waitcnt vmcnt(31)
	v_cvt_pk_bf16_f32 v2, v2, v3
	s_waitcnt lgkmcnt(0)
	v_mfma_f32_16x16x32_bf16 v[134:137], v[144:147], v[148:151], v[134:137]
	v_cvt_pk_bf16_f32 v3, v4, v5
	v_mfma_f32_16x16x32_bf16 v[130:133], v[138:141], v[148:151], v[130:133]
	v_lshl_or_b32 v138, v143, 10, v198
	ds_read_b128 v[138:141], v138
	v_lshl_or_b32 v143, v143, 8, v204
	ds_read_b128 v[144:147], v143
	ds_read_b128 v[148:151], v222
	v_bitop3_b32 v143, v232, 2, 32 bitop3:0xde
	s_waitcnt lgkmcnt(0)
	v_mfma_f32_16x16x32_bf16 v[134:137], v[144:147], v[148:151], v[134:137]
	v_mfma_f32_16x16x32_bf16 v[130:133], v[138:141], v[148:151], v[130:133]
	v_lshl_or_b32 v138, v143, 10, v198
	ds_read_b128 v[138:141], v138
	v_lshl_or_b32 v143, v143, 8, v204
	ds_read_b128 v[144:147], v143
	ds_read_b128 v[148:151], v221
	v_bitop3_b32 v143, v232, 3, 32 bitop3:0xde
	s_waitcnt lgkmcnt(0)
	v_mfma_f32_16x16x32_bf16 v[130:133], v[138:141], v[148:151], v[130:133]
	v_lshl_or_b32 v138, v143, 10, v198
	ds_read_b128 v[138:141], v138
	v_lshl_or_b32 v143, v143, 8, v204
	v_mfma_f32_16x16x32_bf16 v[134:137], v[144:147], v[148:151], v[134:137]
	ds_read_b128 v[144:147], v143
	ds_read_b128 v[148:151], v219
	v_bitop3_b32 v143, v232, 4, 32 bitop3:0xde
	s_waitcnt lgkmcnt(0)
	v_mfma_f32_16x16x32_bf16 v[130:133], v[138:141], v[148:151], v[130:133]
	v_lshl_or_b32 v138, v143, 10, v198
	ds_read_b128 v[138:141], v138
	v_lshl_or_b32 v143, v143, 8, v204
	v_mfma_f32_16x16x32_bf16 v[134:137], v[144:147], v[148:151], v[134:137]
	ds_read_b128 v[144:147], v143
	ds_read_b128 v[148:151], v218
	v_bitop3_b32 v143, v232, 5, 32 bitop3:0xde
	s_waitcnt lgkmcnt(0)
	v_mfma_f32_16x16x32_bf16 v[130:133], v[138:141], v[148:151], v[130:133]
	v_lshl_or_b32 v138, v143, 10, v198
	ds_read_b128 v[138:141], v138
	v_lshl_or_b32 v143, v143, 8, v204
	v_mfma_f32_16x16x32_bf16 v[134:137], v[144:147], v[148:151], v[134:137]
	ds_read_b128 v[144:147], v143
	ds_read_b128 v[148:151], v217
	v_bitop3_b32 v143, v232, 6, 32 bitop3:0xde
	s_waitcnt lgkmcnt(0)
	v_mfma_f32_16x16x32_bf16 v[130:133], v[138:141], v[148:151], v[130:133]
	v_lshl_or_b32 v138, v143, 10, v198
	ds_read_b128 v[138:141], v138
	v_lshl_or_b32 v143, v143, 8, v204
	v_mfma_f32_16x16x32_bf16 v[134:137], v[144:147], v[148:151], v[134:137]
	ds_read_b128 v[144:147], v143
	ds_read_b128 v[148:151], v216
	v_bitop3_b32 v143, v232, 7, 32 bitop3:0xde
	s_waitcnt lgkmcnt(0)
	v_mfma_f32_16x16x32_bf16 v[130:133], v[138:141], v[148:151], v[130:133]
	v_lshl_or_b32 v138, v143, 10, v198
	v_lshl_or_b32 v143, v143, 8, v204
	ds_read_b128 v[138:141], v138
	v_mfma_f32_16x16x32_bf16 v[134:137], v[144:147], v[148:151], v[134:137]
	ds_read_b128 v[144:147], v143
	ds_read_b128 v[148:151], v213
	ds_write_b64 v212, v[2:3]
	s_waitcnt vmcnt(21)
	v_cvt_pk_bf16_f32 v2, v10, v11
	v_cvt_pk_bf16_f32 v3, v12, v13
	ds_write_b64 v211, v[2:3] offset:512
	s_waitcnt vmcnt(20)
	v_cvt_pk_bf16_f32 v2, v14, v15
	v_cvt_pk_bf16_f32 v3, v16, v17
	ds_write_b64 v210, v[2:3] offset:1024
	s_waitcnt vmcnt(19)
	v_cvt_pk_bf16_f32 v2, v22, v23
	v_cvt_pk_bf16_f32 v3, v24, v25
	ds_write_b64 v209, v[2:3] offset:1536
	s_waitcnt vmcnt(18)
	v_cvt_pk_bf16_f32 v2, v30, v31
	v_cvt_pk_bf16_f32 v3, v32, v33
	ds_write_b64 v208, v[2:3] offset:2048
	s_waitcnt vmcnt(17)
	v_cvt_pk_bf16_f32 v2, v38, v39
	v_cvt_pk_bf16_f32 v3, v40, v41
	ds_write_b64 v207, v[2:3] offset:2560
	s_waitcnt vmcnt(16)
	v_cvt_pk_bf16_f32 v2, v46, v47
	v_cvt_pk_bf16_f32 v3, v48, v49
	ds_write_b64 v206, v[2:3] offset:3072
	v_cvt_pk_bf16_f32 v2, v54, v55
	v_cvt_pk_bf16_f32 v3, v56, v57
	ds_write_b64 v205, v[2:3] offset:3584
	v_cvt_pk_bf16_f32 v2, v62, v63
	v_cvt_pk_bf16_f32 v3, v64, v65
	ds_write_b64 v231, v[2:3] offset:4096
	v_cvt_pk_bf16_f32 v2, v70, v71
	v_cvt_pk_bf16_f32 v3, v72, v73
	ds_write_b64 v230, v[2:3] offset:4608
	v_cvt_pk_bf16_f32 v2, v78, v79
	v_cvt_pk_bf16_f32 v3, v80, v81
	ds_write_b64 v229, v[2:3] offset:5120
	v_cvt_pk_bf16_f32 v2, v86, v87
	v_cvt_pk_bf16_f32 v3, v88, v89
	ds_write_b64 v228, v[2:3] offset:5632
	v_cvt_pk_bf16_f32 v2, v94, v95
	v_cvt_pk_bf16_f32 v3, v96, v97
	ds_write_b64 v227, v[2:3] offset:6144
	v_cvt_pk_bf16_f32 v2, v106, v107
	v_cvt_pk_bf16_f32 v3, v108, v109
	ds_write_b64 v226, v[2:3] offset:6656
	v_cvt_pk_bf16_f32 v2, v114, v115
	v_cvt_pk_bf16_f32 v3, v116, v117
	ds_write_b64 v225, v[2:3] offset:7168
	v_cvt_pk_bf16_f32 v2, v122, v123
	v_cvt_pk_bf16_f32 v3, v124, v125
	ds_write_b64 v224, v[2:3] offset:7680
	v_lshlrev_b32_e32 v2, 10, v142
	v_and_or_b32 v2, v2, s0, v203
	v_or_b32_e32 v3, 0x2000, v2
	buffer_load_dwordx4 v[10:13], v2, s[4:7], 0 offen nt
	buffer_load_dwordx4 v[14:17], v3, s[4:7], 0 offen nt
	v_or_b32_e32 v3, 0x4000, v2
	buffer_load_dwordx4 v[22:25], v3, s[4:7], 0 offen nt
	v_or_b32_e32 v3, 0x6000, v2
	buffer_load_dwordx4 v[30:33], v3, s[4:7], 0 offen nt
	v_or_b32_e32 v3, 0x8000, v2
	buffer_load_dwordx4 v[38:41], v3, s[4:7], 0 offen nt
	v_or_b32_e32 v3, 0xa000, v2
	buffer_load_dwordx4 v[46:49], v3, s[4:7], 0 offen nt
	v_or_b32_e32 v3, 0xc000, v2
	buffer_load_dwordx4 v[54:57], v3, s[4:7], 0 offen nt
	v_or_b32_e32 v3, 0xe000, v2
	buffer_load_dwordx4 v[62:65], v3, s[4:7], 0 offen nt
	v_or_b32_e32 v3, 0x10000, v2
	buffer_load_dwordx4 v[70:73], v3, s[4:7], 0 offen nt
	v_or_b32_e32 v3, 0x12000, v2
	buffer_load_dwordx4 v[78:81], v3, s[4:7], 0 offen nt
	v_or_b32_e32 v3, 0x14000, v2
	buffer_load_dwordx4 v[86:89], v3, s[4:7], 0 offen nt
	v_or_b32_e32 v3, 0x16000, v2
	buffer_load_dwordx4 v[94:97], v3, s[4:7], 0 offen nt
	v_or_b32_e32 v3, 0x18000, v2
	buffer_load_dwordx4 v[106:109], v3, s[4:7], 0 offen nt
	v_or_b32_e32 v3, 0x1a000, v2
	buffer_load_dwordx4 v[114:117], v3, s[4:7], 0 offen nt
	v_or_b32_e32 v3, 0x1c000, v2
	v_or_b32_e32 v2, 0x1e000, v2
	s_waitcnt lgkmcnt(14)
	v_mfma_f32_16x16x32_bf16 v[138:141], v[138:141], v[148:151], v[130:133]
	buffer_load_dwordx4 v[122:125], v3, s[4:7], 0 offen nt
	s_nop 1
	buffer_load_dwordx4 v[130:133], v2, s[4:7], 0 offen nt
	v_mfma_f32_16x16x32_bf16 v[134:137], v[144:147], v[148:151], v[134:137]
	v_lshlrev_b32_e32 v2, 3, v234
	v_and_b32_e32 v143, 56, v2
	v_lshl_or_b32 v2, v143, 10, v198
	v_lshl_or_b32 v152, v143, 8, v204
	ds_read_b128 v[2:5], v2
	ds_read_b128 v[144:147], v223
	ds_read_b128 v[148:151], v222
	ds_read_b128 v[152:155], v152
	v_or_b32_e32 v156, 1, v143
	v_lshl_or_b32 v157, v156, 10, v198
	s_waitcnt lgkmcnt(2)
	v_mfma_f32_16x16x32_bf16 v[2:5], v[2:5], v[144:147], v[138:141]
	s_waitcnt vmcnt(31)
	v_cvt_pk_bf16_f32 v6, v6, v7
	v_cvt_pk_bf16_f32 v7, v8, v9
	s_waitcnt lgkmcnt(0)
	v_mfma_f32_16x16x32_bf16 v[134:137], v[152:155], v[144:147], v[134:137]
	ds_read_b128 v[138:141], v157
	v_lshl_or_b32 v144, v156, 8, v204
	ds_read_b128 v[144:147], v144
	v_or_b32_e32 v156, 2, v143
	s_waitcnt lgkmcnt(1)
	v_mfma_f32_16x16x32_bf16 v[2:5], v[138:141], v[148:151], v[2:5]
	v_lshl_or_b32 v138, v156, 10, v198
	ds_read_b128 v[138:141], v138
	ds_read_b128 v[152:155], v221
	s_waitcnt lgkmcnt(2)
	v_mfma_f32_16x16x32_bf16 v[134:137], v[144:147], v[148:151], v[134:137]
	v_lshl_or_b32 v144, v156, 8, v204
	v_or_b32_e32 v156, 3, v143
	ds_read_b128 v[144:147], v144
	ds_read_b128 v[148:151], v219
	s_waitcnt lgkmcnt(2)
	v_mfma_f32_16x16x32_bf16 v[2:5], v[138:141], v[152:155], v[2:5]
	v_lshl_or_b32 v138, v156, 10, v198
	ds_read_b128 v[138:141], v138
	s_waitcnt lgkmcnt(2)
	v_mfma_f32_16x16x32_bf16 v[134:137], v[144:147], v[152:155], v[134:137]
	v_lshl_or_b32 v144, v156, 8, v204
	ds_read_b128 v[144:147], v144
	v_or_b32_e32 v152, 4, v143
	s_waitcnt lgkmcnt(1)
	v_mfma_f32_16x16x32_bf16 v[2:5], v[138:141], v[148:151], v[2:5]
	v_lshl_or_b32 v138, v152, 10, v198
	ds_read_b128 v[138:141], v138
	v_or_b32_e32 v156, 5, v143
	s_waitcnt lgkmcnt(1)
	v_mfma_f32_16x16x32_bf16 v[134:137], v[144:147], v[148:151], v[134:137]
	ds_read_b128 v[144:147], v218
	v_lshl_or_b32 v148, v152, 8, v204
	ds_read_b128 v[148:151], v148
	ds_read_b128 v[152:155], v217
	s_waitcnt lgkmcnt(2)
	v_mfma_f32_16x16x32_bf16 v[2:5], v[138:141], v[144:147], v[2:5]
	v_lshl_or_b32 v138, v156, 10, v198
	ds_read_b128 v[138:141], v138
	s_waitcnt lgkmcnt(2)
	v_mfma_f32_16x16x32_bf16 v[134:137], v[148:151], v[144:147], v[134:137]
	v_lshl_or_b32 v144, v156, 8, v204
	ds_read_b128 v[144:147], v144
	v_or_b32_e32 v148, 6, v143
	s_waitcnt lgkmcnt(1)
	v_mfma_f32_16x16x32_bf16 v[2:5], v[138:141], v[152:155], v[2:5]
	v_lshl_or_b32 v138, v148, 10, v198
	ds_read_b128 v[138:141], v138
	v_lshl_or_b32 v148, v148, 8, v204
	s_waitcnt lgkmcnt(1)
	v_mfma_f32_16x16x32_bf16 v[134:137], v[144:147], v[152:155], v[134:137]
	ds_read_b128 v[144:147], v216
	ds_read_b128 v[148:151], v148
	ds_read_b128 v[152:155], v213
	v_or_b32_e32 v143, 7, v143
	ds_write_b64 v212, v[6:7]
	s_waitcnt lgkmcnt(3)
	v_mfma_f32_16x16x32_bf16 v[2:5], v[138:141], v[144:147], v[2:5]
	v_lshl_or_b32 v138, v143, 10, v198
	v_lshl_or_b32 v143, v143, 8, v204
	s_waitcnt vmcnt(19)
	v_cvt_pk_bf16_f32 v6, v18, v19
	v_cvt_pk_bf16_f32 v7, v20, v21
	ds_read_b128 v[138:141], v138
	s_waitcnt lgkmcnt(3)
	v_mfma_f32_16x16x32_bf16 v[134:137], v[148:151], v[144:147], v[134:137]
	ds_read_b128 v[144:147], v143
	ds_write_b64 v211, v[6:7] offset:512
	s_waitcnt vmcnt(18)
	v_cvt_pk_bf16_f32 v6, v26, v27
	v_cvt_pk_bf16_f32 v7, v28, v29
	ds_write_b64 v210, v[6:7] offset:1024
	s_waitcnt vmcnt(17)
	v_cvt_pk_bf16_f32 v6, v34, v35
	v_cvt_pk_bf16_f32 v7, v36, v37
	ds_write_b64 v209, v[6:7] offset:1536
	s_waitcnt vmcnt(16)
	v_cvt_pk_bf16_f32 v6, v42, v43
	v_cvt_pk_bf16_f32 v7, v44, v45
	ds_write_b64 v208, v[6:7] offset:2048
	v_cvt_pk_bf16_f32 v6, v50, v51
	v_cvt_pk_bf16_f32 v7, v52, v53
	ds_write_b64 v207, v[6:7] offset:2560
	v_cvt_pk_bf16_f32 v6, v58, v59
	v_cvt_pk_bf16_f32 v7, v60, v61
	ds_write_b64 v206, v[6:7] offset:3072
	v_cvt_pk_bf16_f32 v6, v66, v67
	v_cvt_pk_bf16_f32 v7, v68, v69
	ds_write_b64 v205, v[6:7] offset:3584
	v_cvt_pk_bf16_f32 v6, v74, v75
	v_cvt_pk_bf16_f32 v7, v76, v77
	ds_write_b64 v231, v[6:7] offset:4096
	v_cvt_pk_bf16_f32 v6, v82, v83
	v_cvt_pk_bf16_f32 v7, v84, v85
	ds_write_b64 v230, v[6:7] offset:4608
	v_cvt_pk_bf16_f32 v6, v90, v91
	v_cvt_pk_bf16_f32 v7, v92, v93
	s_waitcnt lgkmcnt(9)
	v_mfma_f32_16x16x32_bf16 v[134:137], v[144:147], v[152:155], v[134:137]
	ds_write_b64 v229, v[6:7] offset:5120
	v_cvt_pk_bf16_f32 v6, v98, v99
	v_cvt_pk_bf16_f32 v7, v100, v101
	ds_write_b64 v228, v[6:7] offset:5632
	v_cvt_pk_bf16_f32 v6, v102, v103
	v_cvt_pk_bf16_f32 v7, v104, v105
	ds_write_b64 v227, v[6:7] offset:6144
	v_cvt_pk_bf16_f32 v6, v110, v111
	v_cvt_pk_bf16_f32 v7, v112, v113
	ds_write_b64 v226, v[6:7] offset:6656
	v_cvt_pk_bf16_f32 v6, v118, v119
	v_cvt_pk_bf16_f32 v7, v120, v121
	v_mfma_f32_16x16x32_bf16 v[2:5], v[138:141], v[152:155], v[2:5]
	ds_write_b64 v225, v[6:7] offset:7168
	v_cvt_pk_bf16_f32 v6, v126, v127
	v_cvt_pk_bf16_f32 v7, v128, v129
	ds_write_b64 v224, v[6:7] offset:7680
	v_add_u32_e32 v6, 48, v232
	v_and_b32_e32 v50, 56, v6
	v_lshl_or_b32 v6, v50, 10, v198
	v_lshl_or_b32 v34, v50, 8, v204
	ds_read_b128 v[6:9], v6
	ds_read_b128 v[18:21], v223
	ds_read_b128 v[26:29], v222
	ds_read_b128 v[34:37], v34
	v_or_b32_e32 v42, 1, v50
	v_lshl_or_b32 v43, v42, 10, v198
	s_waitcnt lgkmcnt(2)
	v_mfma_f32_16x16x32_bf16 v[2:5], v[6:9], v[18:21], v[2:5]
	ds_read_b128 v[6:9], v43
	v_or_b32_e32 v51, 2, v50
	s_waitcnt lgkmcnt(1)
	v_mfma_f32_16x16x32_bf16 v[18:21], v[34:37], v[18:21], v[134:137]
	v_lshl_or_b32 v34, v42, 8, v204
	ds_read_b128 v[34:37], v34
	s_waitcnt lgkmcnt(1)
	v_mfma_f32_16x16x32_bf16 v[2:5], v[6:9], v[26:29], v[2:5]
	v_lshl_or_b32 v6, v51, 10, v198
	ds_read_b128 v[6:9], v6
	ds_read_b128 v[42:45], v221
	s_waitcnt lgkmcnt(2)
	v_mfma_f32_16x16x32_bf16 v[18:21], v[34:37], v[26:29], v[18:21]
	v_lshl_or_b32 v26, v51, 8, v204
	v_or_b32_e32 v51, 3, v50
	ds_read_b128 v[26:29], v26
	ds_read_b128 v[34:37], v219
	s_waitcnt lgkmcnt(2)
	v_mfma_f32_16x16x32_bf16 v[2:5], v[6:9], v[42:45], v[2:5]
	v_lshl_or_b32 v6, v51, 10, v198
	ds_read_b128 v[6:9], v6
	s_waitcnt lgkmcnt(2)
	v_mfma_f32_16x16x32_bf16 v[18:21], v[26:29], v[42:45], v[18:21]
	v_lshl_or_b32 v26, v51, 8, v204
	ds_read_b128 v[26:29], v26
	v_or_b32_e32 v42, 4, v50
	s_waitcnt lgkmcnt(1)
	v_mfma_f32_16x16x32_bf16 v[2:5], v[6:9], v[34:37], v[2:5]
	v_lshl_or_b32 v6, v42, 10, v198
	ds_read_b128 v[6:9], v6
	v_or_b32_e32 v51, 5, v50
	s_waitcnt lgkmcnt(1)
	v_mfma_f32_16x16x32_bf16 v[18:21], v[26:29], v[34:37], v[18:21]
	ds_read_b128 v[26:29], v218
	v_lshl_or_b32 v34, v42, 8, v204
	ds_read_b128 v[34:37], v34
	ds_read_b128 v[42:45], v217
	s_waitcnt lgkmcnt(2)
	v_mfma_f32_16x16x32_bf16 v[2:5], v[6:9], v[26:29], v[2:5]
	v_lshl_or_b32 v6, v51, 10, v198
	ds_read_b128 v[6:9], v6
	s_waitcnt lgkmcnt(2)
	v_mfma_f32_16x16x32_bf16 v[18:21], v[34:37], v[26:29], v[18:21]
	v_lshl_or_b32 v26, v51, 8, v204
	ds_read_b128 v[26:29], v26
	v_or_b32_e32 v34, 6, v50
	s_waitcnt lgkmcnt(1)
	v_mfma_f32_16x16x32_bf16 v[2:5], v[6:9], v[42:45], v[2:5]
	v_lshl_or_b32 v6, v34, 10, v198
	ds_read_b128 v[6:9], v6
	v_lshl_or_b32 v34, v34, 8, v204
	s_waitcnt lgkmcnt(1)
	v_mfma_f32_16x16x32_bf16 v[18:21], v[26:29], v[42:45], v[18:21]
	ds_read_b128 v[26:29], v216
	ds_read_b128 v[34:37], v34
	ds_read_b128 v[42:45], v213
	v_or_b32_e32 v50, 7, v50
	s_waitcnt lgkmcnt(2)
	v_mfma_f32_16x16x32_bf16 v[2:5], v[6:9], v[26:29], v[2:5]
	v_lshl_or_b32 v6, v50, 10, v198
	ds_read_b128 v[6:9], v6
	s_waitcnt lgkmcnt(2)
	v_mfma_f32_16x16x32_bf16 v[18:21], v[34:37], v[26:29], v[18:21]
	v_lshl_or_b32 v26, v50, 8, v204
	ds_read_b128 v[26:29], v26
	s_waitcnt lgkmcnt(1)
	v_mfma_f32_16x16x32_bf16 v[34:37], v[6:9], v[42:45], v[2:5]
	v_and_b32_e32 v74, 7, v197
	v_lshrrev_b32_e32 v75, 3, v197
	v_lshlrev_b32_e32 v192, 13, v200
	v_lshlrev_b32_e32 v193, 11, v200
	v_lshl_add_u32 v203, v197, 2, v196
	v_lshl_or_b32 v192, v75, 8, v192
	v_lshl_or_b32 v193, v75, 6, v193
	v_add_u32_e32 v203, 0x24800, v203
	v_lshl_or_b32 v192, v201, 6, v192
	v_lshl_or_b32 v193, v74, 1, v193
	v_lshl_or_b32 v192, v74, 1, v192
	v_or_b32_e32 v193, 0x10000, v193
	v_cmp_gt_u32_e64 s[36:37], 16, v1
	v_cmp_eq_u32_e64 s[38:39], 1, v201
	ds_read2_b32 v[2:3], v203 offset1:16
	ds_read2_b32 v[4:5], v203 offset0:32 offset1:48
	ds_read2_b32 v[6:7], v203 offset0:64 offset1:80
	ds_read2_b32 v[8:9], v203 offset0:96 offset1:112
	ds_read2_b32 v[50:51], v203 offset0:128 offset1:144
	ds_read2_b32 v[52:53], v203 offset0:160 offset1:176
	ds_read2_b32 v[58:59], v203 offset0:192 offset1:208
	ds_read2_b32 v[60:61], v203 offset0:224 offset1:240
	v_mov_b32_e32 v146, 0
	v_mov_b32_e32 v147, 0
	v_mov_b32_e32 v150, 0
	v_mov_b32_e32 v151, 0
	v_mov_b32_e32 v154, 0
	v_mov_b32_e32 v155, 0
	v_mov_b32_e32 v158, 0
	v_mov_b32_e32 v159, 0
	v_mov_b32_e32 v162, 0
	v_mov_b32_e32 v163, 0
	v_mov_b32_e32 v166, 0
	v_mov_b32_e32 v167, 0
	v_mov_b32_e32 v170, 0
	v_mov_b32_e32 v171, 0
	v_mov_b32_e32 v174, 0
	v_mov_b32_e32 v175, 0
	v_mov_b32_e32 v178, 0
	v_mov_b32_e32 v179, 0
	v_mov_b32_e32 v182, 0
	v_mov_b32_e32 v183, 0
	v_mov_b32_e32 v186, 0
	v_mov_b32_e32 v187, 0
	v_mov_b32_e32 v190, 0
	v_mov_b32_e32 v191, 0
	v_mov_b32_e32 v234, 0
	v_mov_b32_e32 v235, 0
	v_mov_b32_e32 v238, 0
	v_mov_b32_e32 v239, 0
	v_mov_b32_e32 v242, 0
	v_mov_b32_e32 v243, 0
	v_mov_b32_e32 v246, 0
	v_mov_b32_e32 v247, 0
	ds_read_u16 v82, v192
	ds_read_u16 v83, v192 offset:16
	ds_read_u16 v84, v192 offset:32
	ds_read_u16 v85, v192 offset:48
	ds_read_u16 v90, v193
	ds_read_u16 v91, v193 offset:16
	ds_read_u16 v92, v193 offset:32
	ds_read_u16 v93, v193 offset:48
	ds_read_u16 v98, v192 offset:512
	ds_read_u16 v99, v192 offset:528
	ds_read_u16 v100, v192 offset:544
	ds_read_u16 v101, v192 offset:560
	ds_read_u16 v102, v193 offset:128
	ds_read_u16 v103, v193 offset:144
	ds_read_u16 v104, v193 offset:160
	ds_read_u16 v105, v193 offset:176
	s_waitcnt lgkmcnt(8)
	v_lshl_or_b32 v144, v83, 16, v82
	v_lshl_or_b32 v145, v85, 16, v84
	s_mov_b64 exec, s[36:37]
	v_lshl_or_b32 v146, v91, 16, v90
	v_lshl_or_b32 v147, v93, 16, v92
	s_mov_b64 exec, -1
	ds_read_u16 v82, v192 offset:1024
	ds_read_u16 v83, v192 offset:1040
	ds_read_u16 v84, v192 offset:1056
	ds_read_u16 v85, v192 offset:1072
	ds_read_u16 v90, v193 offset:256
	ds_read_u16 v91, v193 offset:272
	ds_read_u16 v92, v193 offset:288
	ds_read_u16 v93, v193 offset:304
	s_waitcnt lgkmcnt(8)
	v_lshl_or_b32 v148, v99, 16, v98
	v_lshl_or_b32 v149, v101, 16, v100
	s_mov_b64 exec, s[36:37]
	v_lshl_or_b32 v150, v103, 16, v102
	v_lshl_or_b32 v151, v105, 16, v104
	s_mov_b64 exec, -1
	ds_read_u16 v98, v192 offset:1536
	ds_read_u16 v99, v192 offset:1552
	ds_read_u16 v100, v192 offset:1568
	ds_read_u16 v101, v192 offset:1584
	ds_read_u16 v102, v193 offset:384
	ds_read_u16 v103, v193 offset:400
	ds_read_u16 v104, v193 offset:416
	ds_read_u16 v105, v193 offset:432
	s_waitcnt lgkmcnt(8)
	v_lshl_or_b32 v152, v83, 16, v82
	v_lshl_or_b32 v153, v85, 16, v84
	s_mov_b64 exec, s[36:37]
	v_lshl_or_b32 v154, v91, 16, v90
	v_lshl_or_b32 v155, v93, 16, v92
	s_mov_b64 exec, -1
	ds_read_u16 v82, v192 offset:2048
	ds_read_u16 v83, v192 offset:2064
	ds_read_u16 v84, v192 offset:2080
	ds_read_u16 v85, v192 offset:2096
	ds_read_u16 v90, v193 offset:512
	ds_read_u16 v91, v193 offset:528
	ds_read_u16 v92, v193 offset:544
	ds_read_u16 v93, v193 offset:560
	s_waitcnt lgkmcnt(8)
	v_lshl_or_b32 v156, v99, 16, v98
	v_lshl_or_b32 v157, v101, 16, v100
	s_mov_b64 exec, s[36:37]
	v_lshl_or_b32 v158, v103, 16, v102
	v_lshl_or_b32 v159, v105, 16, v104
	s_mov_b64 exec, -1
	ds_read_u16 v98, v192 offset:2560
	ds_read_u16 v99, v192 offset:2576
	ds_read_u16 v100, v192 offset:2592
	ds_read_u16 v101, v192 offset:2608
	ds_read_u16 v102, v193 offset:640
	ds_read_u16 v103, v193 offset:656
	ds_read_u16 v104, v193 offset:672
	ds_read_u16 v105, v193 offset:688
	s_waitcnt lgkmcnt(8)
	v_lshl_or_b32 v160, v83, 16, v82
	v_lshl_or_b32 v161, v85, 16, v84
	s_mov_b64 exec, s[36:37]
	v_lshl_or_b32 v162, v91, 16, v90
	v_lshl_or_b32 v163, v93, 16, v92
	s_mov_b64 exec, -1
	ds_read_u16 v82, v192 offset:3072
	ds_read_u16 v83, v192 offset:3088
	ds_read_u16 v84, v192 offset:3104
	ds_read_u16 v85, v192 offset:3120
	ds_read_u16 v90, v193 offset:768
	ds_read_u16 v91, v193 offset:784
	ds_read_u16 v92, v193 offset:800
	ds_read_u16 v93, v193 offset:816
	s_waitcnt lgkmcnt(8)
	v_lshl_or_b32 v164, v99, 16, v98
	v_lshl_or_b32 v165, v101, 16, v100
	s_mov_b64 exec, s[36:37]
	v_lshl_or_b32 v166, v103, 16, v102
	v_lshl_or_b32 v167, v105, 16, v104
	s_mov_b64 exec, -1
	ds_read_u16 v98, v192 offset:3584
	ds_read_u16 v99, v192 offset:3600
	ds_read_u16 v100, v192 offset:3616
	ds_read_u16 v101, v192 offset:3632
	ds_read_u16 v102, v193 offset:896
	ds_read_u16 v103, v193 offset:912
	ds_read_u16 v104, v193 offset:928
	ds_read_u16 v105, v193 offset:944
	s_waitcnt lgkmcnt(8)
	v_lshl_or_b32 v168, v83, 16, v82
	v_lshl_or_b32 v169, v85, 16, v84
	s_mov_b64 exec, s[36:37]
	v_lshl_or_b32 v170, v91, 16, v90
	v_lshl_or_b32 v171, v93, 16, v92
	s_mov_b64 exec, -1
	ds_read_u16 v82, v192 offset:4096
	ds_read_u16 v83, v192 offset:4112
	ds_read_u16 v84, v192 offset:4128
	ds_read_u16 v85, v192 offset:4144
	ds_read_u16 v90, v193 offset:1024
	ds_read_u16 v91, v193 offset:1040
	ds_read_u16 v92, v193 offset:1056
	ds_read_u16 v93, v193 offset:1072
	s_waitcnt lgkmcnt(8)
	v_lshl_or_b32 v172, v99, 16, v98
	v_lshl_or_b32 v173, v101, 16, v100
	s_mov_b64 exec, s[36:37]
	v_lshl_or_b32 v174, v103, 16, v102
	v_lshl_or_b32 v175, v105, 16, v104
	s_mov_b64 exec, -1
	ds_read_u16 v98, v192 offset:4608
	ds_read_u16 v99, v192 offset:4624
	ds_read_u16 v100, v192 offset:4640
	ds_read_u16 v101, v192 offset:4656
	ds_read_u16 v102, v193 offset:1152
	ds_read_u16 v103, v193 offset:1168
	ds_read_u16 v104, v193 offset:1184
	ds_read_u16 v105, v193 offset:1200
	s_waitcnt lgkmcnt(8)
	v_lshl_or_b32 v176, v83, 16, v82
	v_lshl_or_b32 v177, v85, 16, v84
	s_mov_b64 exec, s[36:37]
	v_lshl_or_b32 v178, v91, 16, v90
	v_lshl_or_b32 v179, v93, 16, v92
	s_mov_b64 exec, -1
	ds_read_u16 v82, v192 offset:5120
	ds_read_u16 v83, v192 offset:5136
	ds_read_u16 v84, v192 offset:5152
	ds_read_u16 v85, v192 offset:5168
	ds_read_u16 v90, v193 offset:1280
	ds_read_u16 v91, v193 offset:1296
	ds_read_u16 v92, v193 offset:1312
	ds_read_u16 v93, v193 offset:1328
	s_waitcnt lgkmcnt(8)
	v_lshl_or_b32 v180, v99, 16, v98
	v_lshl_or_b32 v181, v101, 16, v100
	s_mov_b64 exec, s[36:37]
	v_lshl_or_b32 v182, v103, 16, v102
	v_lshl_or_b32 v183, v105, 16, v104
	s_mov_b64 exec, -1
	ds_read_u16 v98, v192 offset:5632
	ds_read_u16 v99, v192 offset:5648
	ds_read_u16 v100, v192 offset:5664
	ds_read_u16 v101, v192 offset:5680
	ds_read_u16 v102, v193 offset:1408
	ds_read_u16 v103, v193 offset:1424
	ds_read_u16 v104, v193 offset:1440
	ds_read_u16 v105, v193 offset:1456
	s_waitcnt lgkmcnt(8)
	v_lshl_or_b32 v184, v83, 16, v82
	v_lshl_or_b32 v185, v85, 16, v84
	s_mov_b64 exec, s[36:37]
	v_lshl_or_b32 v186, v91, 16, v90
	v_lshl_or_b32 v187, v93, 16, v92
	s_mov_b64 exec, -1
	ds_read_u16 v82, v192 offset:6144
	ds_read_u16 v83, v192 offset:6160
	ds_read_u16 v84, v192 offset:6176
	ds_read_u16 v85, v192 offset:6192
	ds_read_u16 v90, v193 offset:1536
	ds_read_u16 v91, v193 offset:1552
	ds_read_u16 v92, v193 offset:1568
	ds_read_u16 v93, v193 offset:1584
	s_waitcnt lgkmcnt(8)
	v_lshl_or_b32 v188, v99, 16, v98
	v_lshl_or_b32 v189, v101, 16, v100
	s_mov_b64 exec, s[36:37]
	v_lshl_or_b32 v190, v103, 16, v102
	v_lshl_or_b32 v191, v105, 16, v104
	s_mov_b64 exec, -1
	ds_read_u16 v98, v192 offset:6656
	ds_read_u16 v99, v192 offset:6672
	ds_read_u16 v100, v192 offset:6688
	ds_read_u16 v101, v192 offset:6704
	ds_read_u16 v102, v193 offset:1664
	ds_read_u16 v103, v193 offset:1680
	ds_read_u16 v104, v193 offset:1696
	ds_read_u16 v105, v193 offset:1712
	s_waitcnt lgkmcnt(8)
	v_lshl_or_b32 v232, v83, 16, v82
	v_lshl_or_b32 v233, v85, 16, v84
	s_mov_b64 exec, s[36:37]
	v_lshl_or_b32 v234, v91, 16, v90
	v_lshl_or_b32 v235, v93, 16, v92
	s_mov_b64 exec, -1
	ds_read_u16 v82, v192 offset:7168
	ds_read_u16 v83, v192 offset:7184
	ds_read_u16 v84, v192 offset:7200
	ds_read_u16 v85, v192 offset:7216
	ds_read_u16 v90, v193 offset:1792
	ds_read_u16 v91, v193 offset:1808
	ds_read_u16 v92, v193 offset:1824
	ds_read_u16 v93, v193 offset:1840
	s_waitcnt lgkmcnt(8)
	v_lshl_or_b32 v236, v99, 16, v98
	v_lshl_or_b32 v237, v101, 16, v100
	s_mov_b64 exec, s[36:37]
	v_lshl_or_b32 v238, v103, 16, v102
	v_lshl_or_b32 v239, v105, 16, v104
	s_mov_b64 exec, -1
	ds_read_u16 v98, v192 offset:7680
	ds_read_u16 v99, v192 offset:7696
	ds_read_u16 v100, v192 offset:7712
	ds_read_u16 v101, v192 offset:7728
	ds_read_u16 v102, v193 offset:1920
	ds_read_u16 v103, v193 offset:1936
	ds_read_u16 v104, v193 offset:1952
	ds_read_u16 v105, v193 offset:1968
	s_waitcnt lgkmcnt(8)
	v_lshl_or_b32 v240, v83, 16, v82
	v_lshl_or_b32 v241, v85, 16, v84
	s_mov_b64 exec, s[36:37]
	v_lshl_or_b32 v242, v91, 16, v90
	v_lshl_or_b32 v243, v93, 16, v92
	s_mov_b64 exec, -1
	s_waitcnt lgkmcnt(0)
	v_lshl_or_b32 v244, v99, 16, v98
	v_lshl_or_b32 v245, v101, 16, v100
	s_mov_b64 exec, s[36:37]
	v_lshl_or_b32 v246, v103, 16, v102
	v_lshl_or_b32 v247, v105, 16, v104
	s_mov_b64 exec, -1
	s_waitcnt lgkmcnt(0)
	s_mov_b64 exec, s[38:39]
	v_cvt_pk_bf16_f32 v66, v2, v195
	v_cvt_pk_bf16_f32 v74, v3, v195
	v_lshlrev_b32_e32 v67, 16, v66
	v_lshlrev_b32_e32 v75, 16, v74
	v_sub_f32_e32 v2, v2, v67
	v_sub_f32_e32 v3, v3, v75
	v_cvt_pk_bf16_f32 v68, v2, v195
	v_cvt_pk_bf16_f32 v76, v3, v195
	v_lshlrev_b32_e32 v69, 16, v68
	v_lshlrev_b32_e32 v77, 16, v76
	v_sub_f32_e32 v2, v2, v69
	v_sub_f32_e32 v3, v3, v77
	v_cvt_pk_bf16_f32 v147, v2, v195
	v_cvt_pk_bf16_f32 v151, v3, v195
	v_cvt_pk_bf16_f32 v146, v67, v69
	v_cvt_pk_bf16_f32 v150, v75, v77
	v_cvt_pk_bf16_f32 v66, v4, v195
	v_cvt_pk_bf16_f32 v74, v5, v195
	v_lshlrev_b32_e32 v67, 16, v66
	v_lshlrev_b32_e32 v75, 16, v74
	v_sub_f32_e32 v4, v4, v67
	v_sub_f32_e32 v5, v5, v75
	v_cvt_pk_bf16_f32 v68, v4, v195
	v_cvt_pk_bf16_f32 v76, v5, v195
	v_lshlrev_b32_e32 v69, 16, v68
	v_lshlrev_b32_e32 v77, 16, v76
	v_sub_f32_e32 v4, v4, v69
	v_sub_f32_e32 v5, v5, v77
	v_cvt_pk_bf16_f32 v155, v4, v195
	v_cvt_pk_bf16_f32 v159, v5, v195
	v_cvt_pk_bf16_f32 v154, v67, v69
	v_cvt_pk_bf16_f32 v158, v75, v77
	v_cvt_pk_bf16_f32 v66, v6, v195
	v_cvt_pk_bf16_f32 v74, v7, v195
	v_lshlrev_b32_e32 v67, 16, v66
	v_lshlrev_b32_e32 v75, 16, v74
	v_sub_f32_e32 v6, v6, v67
	v_sub_f32_e32 v7, v7, v75
	v_cvt_pk_bf16_f32 v68, v6, v195
	v_cvt_pk_bf16_f32 v76, v7, v195
	v_lshlrev_b32_e32 v69, 16, v68
	v_lshlrev_b32_e32 v77, 16, v76
	v_sub_f32_e32 v6, v6, v69
	v_sub_f32_e32 v7, v7, v77
	v_cvt_pk_bf16_f32 v163, v6, v195
	v_cvt_pk_bf16_f32 v167, v7, v195
	v_cvt_pk_bf16_f32 v162, v67, v69
	v_cvt_pk_bf16_f32 v166, v75, v77
	v_cvt_pk_bf16_f32 v66, v8, v195
	v_cvt_pk_bf16_f32 v74, v9, v195
	v_lshlrev_b32_e32 v67, 16, v66
	v_lshlrev_b32_e32 v75, 16, v74
	v_sub_f32_e32 v8, v8, v67
	v_sub_f32_e32 v9, v9, v75
	v_cvt_pk_bf16_f32 v68, v8, v195
	v_cvt_pk_bf16_f32 v76, v9, v195
	v_lshlrev_b32_e32 v69, 16, v68
	v_lshlrev_b32_e32 v77, 16, v76
	v_sub_f32_e32 v8, v8, v69
	v_sub_f32_e32 v9, v9, v77
	v_cvt_pk_bf16_f32 v171, v8, v195
	v_cvt_pk_bf16_f32 v175, v9, v195
	v_cvt_pk_bf16_f32 v170, v67, v69
	v_cvt_pk_bf16_f32 v174, v75, v77
	v_cvt_pk_bf16_f32 v66, v50, v195
	v_cvt_pk_bf16_f32 v74, v51, v195
	v_lshlrev_b32_e32 v67, 16, v66
	v_lshlrev_b32_e32 v75, 16, v74
	v_sub_f32_e32 v50, v50, v67
	v_sub_f32_e32 v51, v51, v75
	v_cvt_pk_bf16_f32 v68, v50, v195
	v_cvt_pk_bf16_f32 v76, v51, v195
	v_lshlrev_b32_e32 v69, 16, v68
	v_lshlrev_b32_e32 v77, 16, v76
	v_sub_f32_e32 v50, v50, v69
	v_sub_f32_e32 v51, v51, v77
	v_cvt_pk_bf16_f32 v179, v50, v195
	v_cvt_pk_bf16_f32 v183, v51, v195
	v_cvt_pk_bf16_f32 v178, v67, v69
	v_cvt_pk_bf16_f32 v182, v75, v77
	v_cvt_pk_bf16_f32 v66, v52, v195
	v_cvt_pk_bf16_f32 v74, v53, v195
	v_lshlrev_b32_e32 v67, 16, v66
	v_lshlrev_b32_e32 v75, 16, v74
	v_sub_f32_e32 v52, v52, v67
	v_sub_f32_e32 v53, v53, v75
	v_cvt_pk_bf16_f32 v68, v52, v195
	v_cvt_pk_bf16_f32 v76, v53, v195
	v_lshlrev_b32_e32 v69, 16, v68
	v_lshlrev_b32_e32 v77, 16, v76
	v_sub_f32_e32 v52, v52, v69
	v_sub_f32_e32 v53, v53, v77
	v_cvt_pk_bf16_f32 v187, v52, v195
	v_cvt_pk_bf16_f32 v191, v53, v195
	v_cvt_pk_bf16_f32 v186, v67, v69
	v_cvt_pk_bf16_f32 v190, v75, v77
	v_cvt_pk_bf16_f32 v66, v58, v195
	v_cvt_pk_bf16_f32 v74, v59, v195
	v_lshlrev_b32_e32 v67, 16, v66
	v_lshlrev_b32_e32 v75, 16, v74
	v_sub_f32_e32 v58, v58, v67
	v_sub_f32_e32 v59, v59, v75
	v_cvt_pk_bf16_f32 v68, v58, v195
	v_cvt_pk_bf16_f32 v76, v59, v195
	v_lshlrev_b32_e32 v69, 16, v68
	v_lshlrev_b32_e32 v77, 16, v76
	v_sub_f32_e32 v58, v58, v69
	v_sub_f32_e32 v59, v59, v77
	v_cvt_pk_bf16_f32 v235, v58, v195
	v_cvt_pk_bf16_f32 v239, v59, v195
	v_cvt_pk_bf16_f32 v234, v67, v69
	v_cvt_pk_bf16_f32 v238, v75, v77
	v_cvt_pk_bf16_f32 v66, v60, v195
	v_cvt_pk_bf16_f32 v74, v61, v195
	v_lshlrev_b32_e32 v67, 16, v66
	v_lshlrev_b32_e32 v75, 16, v74
	v_sub_f32_e32 v60, v60, v67
	v_sub_f32_e32 v61, v61, v75
	v_cvt_pk_bf16_f32 v68, v60, v195
	v_cvt_pk_bf16_f32 v76, v61, v195
	v_lshlrev_b32_e32 v69, 16, v68
	v_lshlrev_b32_e32 v77, 16, v76
	v_sub_f32_e32 v60, v60, v69
	v_sub_f32_e32 v61, v61, v77
	v_cvt_pk_bf16_f32 v243, v60, v195
	v_cvt_pk_bf16_f32 v247, v61, v195
	v_cvt_pk_bf16_f32 v242, v67, v69
	v_cvt_pk_bf16_f32 v246, v75, v77
	s_mov_b64 exec, -1
	s_movk_i32 s44, 0x210
	v_and_b32_e32 v192, 48, v0
	v_lshrrev_b32_e32 v193, 5, v1
	v_mad_u32_u24 v214, v197, s44, v199
	v_mad_u32_u24 v215, v193, s44, v199
	v_add_u32_e32 v214, v214, v192
	v_and_b32_e32 v192, 0x1f0, v194
	v_add_u32_e32 v215, v215, v192
	s_and_b32 s44, s2, 7
	s_lshl_b32 s44, s44, 22
	s_lshl_b32 s45, s3, 17
	s_add_i32 s44, s44, s45
	v_lshlrev_b32_e32 v220, 13, v193
	v_or3_b32 v220, s44, v220, v196
	v_add_u32_e32 v220, v220, v192
	v_or_b32_e32 v203, 0x24800, v198
	s_mov_b32 s12, 0
	s_mov_b32 s11, 0x20000
	s_brev_b32 s10, 8
	s_and_b32 s9, s9, 0xffff
	v_lshlrev_b32_e32 v192, 3, v142
	v_and_b32_e32 v192, 56, v192
	v_lshl_or_b32 v193, v192, 8, v204
	v_lshl_or_b32 v192, v192, 10, v198
	s_nop 4
	v_mfma_f32_16x16x32_bf16 v[2:5], v[26:29], v[42:45], v[18:21]
	s_nop 1
	ds_read_b128 v[58:61], v192
	ds_read_b128 v[110:113], v193
	ds_read_b128 v[50:53], v192 offset:1024
	ds_read_b128 v[118:121], v193 offset:256
	ds_read_b128 v[66:69], v192 offset:2048
	ds_read_b128 v[126:129], v193 offset:512
	ds_read_b128 v[74:77], v192 offset:3072
	ds_read_b128 v[134:137], v193 offset:768
	ds_read_b128 v[82:85], v192 offset:4096
	ds_read_b128 v[138:141], v193 offset:1024
	ds_read_b128 v[90:93], v192 offset:5120
	ds_read_b128 v[18:21], v193 offset:1280
	ds_read_b128 v[98:101], v192 offset:6144
	ds_read_b128 v[26:29], v193 offset:1536
	ds_read_b128 v[102:105], v192 offset:7168
	ds_read_b128 v[42:45], v193 offset:1792
	s_waitcnt vmcnt(15)
	v_cvt_pk_bf16_f32 v6, v10, v11
	v_cvt_pk_bf16_f32 v7, v12, v13
	ds_write_b64 v212, v[6:7]
	s_waitcnt vmcnt(14)
	v_cvt_pk_bf16_f32 v6, v14, v15
	v_cvt_pk_bf16_f32 v7, v16, v17
	ds_write_b64 v211, v[6:7] offset:512
	s_waitcnt vmcnt(13)
	v_cvt_pk_bf16_f32 v6, v22, v23
	v_cvt_pk_bf16_f32 v7, v24, v25
	ds_write_b64 v210, v[6:7] offset:1024
	s_waitcnt vmcnt(12)
	v_cvt_pk_bf16_f32 v6, v30, v31
	v_cvt_pk_bf16_f32 v7, v32, v33
	ds_write_b64 v209, v[6:7] offset:1536
	s_waitcnt vmcnt(11)
	v_cvt_pk_bf16_f32 v6, v38, v39
	v_cvt_pk_bf16_f32 v7, v40, v41
	ds_write_b64 v208, v[6:7] offset:2048
	s_waitcnt vmcnt(10)
	v_cvt_pk_bf16_f32 v6, v46, v47
	v_cvt_pk_bf16_f32 v7, v48, v49
	ds_write_b64 v207, v[6:7] offset:2560
	s_waitcnt vmcnt(9)
	v_cvt_pk_bf16_f32 v6, v54, v55
	v_cvt_pk_bf16_f32 v7, v56, v57
	ds_write_b64 v206, v[6:7] offset:3072
	s_waitcnt vmcnt(8)
	v_cvt_pk_bf16_f32 v6, v62, v63
	v_cvt_pk_bf16_f32 v7, v64, v65
	ds_write_b64 v205, v[6:7] offset:3584
	s_waitcnt vmcnt(7)
	v_cvt_pk_bf16_f32 v6, v70, v71
	v_cvt_pk_bf16_f32 v7, v72, v73
	ds_write_b64 v231, v[6:7] offset:4096
	s_waitcnt vmcnt(6)
	v_cvt_pk_bf16_f32 v6, v78, v79
	v_cvt_pk_bf16_f32 v7, v80, v81
	ds_write_b64 v230, v[6:7] offset:4608
	s_waitcnt vmcnt(5)
	v_cvt_pk_bf16_f32 v6, v86, v87
	v_cvt_pk_bf16_f32 v7, v88, v89
	ds_write_b64 v229, v[6:7] offset:5120
	s_waitcnt vmcnt(4)
	v_cvt_pk_bf16_f32 v6, v94, v95
	v_cvt_pk_bf16_f32 v7, v96, v97
	ds_write_b64 v228, v[6:7] offset:5632
	s_waitcnt vmcnt(3)
	v_cvt_pk_bf16_f32 v6, v106, v107
	v_cvt_pk_bf16_f32 v7, v108, v109
	ds_write_b64 v227, v[6:7] offset:6144
	s_waitcnt vmcnt(2)
	v_cvt_pk_bf16_f32 v6, v114, v115
	v_cvt_pk_bf16_f32 v7, v116, v117
	ds_write_b64 v226, v[6:7] offset:6656
	s_waitcnt vmcnt(1)
	v_cvt_pk_bf16_f32 v6, v122, v123
	v_cvt_pk_bf16_f32 v7, v124, v125
	ds_write_b64 v225, v[6:7] offset:7168
	s_waitcnt vmcnt(0)
	v_cvt_pk_bf16_f32 v6, v130, v131
	v_cvt_pk_bf16_f32 v7, v132, v133
	ds_write_b64 v224, v[6:7] offset:7680
	ds_read_b128 v[54:57], v223
	ds_read_b128 v[62:65], v222
	ds_read_b128 v[10:13], v221
	ds_read_b128 v[14:17], v219
	ds_read_b128 v[22:25], v218
	ds_read_b128 v[30:33], v217
	ds_read_b128 v[38:41], v216
	ds_read_b128 v[46:49], v213
	s_waitcnt lgkmcnt(7)
	v_mfma_f32_16x16x32_bf16 v[34:37], v[58:61], v[54:57], v[34:37]
	v_mfma_f32_16x16x32_bf16 v[2:5], v[110:113], v[54:57], v[2:5]
	s_waitcnt lgkmcnt(6)
	v_mfma_f32_16x16x32_bf16 v[34:37], v[50:53], v[62:65], v[34:37]
	v_mfma_f32_16x16x32_bf16 v[2:5], v[118:121], v[62:65], v[2:5]
	s_waitcnt lgkmcnt(5)
	v_mfma_f32_16x16x32_bf16 v[34:37], v[66:69], v[10:13], v[34:37]
	v_mfma_f32_16x16x32_bf16 v[2:5], v[126:129], v[10:13], v[2:5]
	s_waitcnt lgkmcnt(4)
	v_mfma_f32_16x16x32_bf16 v[34:37], v[74:77], v[14:17], v[34:37]
	v_mfma_f32_16x16x32_bf16 v[2:5], v[134:137], v[14:17], v[2:5]
	s_waitcnt lgkmcnt(3)
	v_mfma_f32_16x16x32_bf16 v[34:37], v[82:85], v[22:25], v[34:37]
	v_mfma_f32_16x16x32_bf16 v[2:5], v[138:141], v[22:25], v[2:5]
	s_waitcnt lgkmcnt(2)
	v_mfma_f32_16x16x32_bf16 v[34:37], v[90:93], v[30:33], v[34:37]
	v_mfma_f32_16x16x32_bf16 v[2:5], v[18:21], v[30:33], v[2:5]
	s_waitcnt lgkmcnt(1)
	v_mfma_f32_16x16x32_bf16 v[34:37], v[98:101], v[38:41], v[34:37]
	v_mfma_f32_16x16x32_bf16 v[2:5], v[26:29], v[38:41], v[2:5]
	s_waitcnt lgkmcnt(0)
	v_mfma_f32_16x16x32_bf16 v[56:59], v[102:105], v[46:49], v[34:37]
	v_mfma_f32_16x16x32_bf16 v[60:63], v[42:45], v[46:49], v[2:5]
	v_add_u32_e32 v76, 0x24800, v196
	s_waitcnt lgkmcnt(0)
	v_cmp_gt_u32_e64 s[0:1], 16, v1
	v_cmp_lt_u32_e32 vcc, 15, v1
	s_waitcnt lgkmcnt(0)
	s_nop 2
	v_max_f32_e32 v2, v59, v59
	v_max_f32_e32 v3, v58, v58
	s_waitcnt lgkmcnt(0)
	v_max_f32_e32 v2, v3, v2
	s_nop 0
	s_nop 0
	s_nop 0
	s_waitcnt lgkmcnt(0)
	s_nop 0
	s_nop 0
	s_and_saveexec_b64 s[4:5], vcc
	s_xor_b64 s[4:5], exec, s[4:5]
	s_or_saveexec_b64 s[4:5], s[4:5]
	v_max3_f32 v53, v56, v57, v2
	s_xor_b64 exec, exec, s[4:5]
	v_max_f32_e32 v2, v61, v61
	v_max_f32_e32 v3, v60, v60
	v_max_f32_e32 v2, v3, v2
	v_max_f32_e32 v3, v63, v63
	v_max_f32_e32 v4, v62, v62
	v_max_f32_e32 v3, v4, v3
	v_max3_f32 v53, v53, v2, v3
	s_or_b64 exec, exec, s[4:5]
	v_cmp_eq_u32_e64 s[4:5], 1, v201
	v_max_f32_e32 v53, v53, v53
	v_mov_b32_e32 v68, v53
	s_nop 1
	v_permlane16_swap_b32_e32 v53, v68
	v_max_f32_e32 v68, v53, v68
	v_mov_b32_e32 v55, v68
	s_nop 1
	v_permlane32_swap_b32_e32 v68, v55
	v_max_f32_e32 v68, v68, v55
	v_sub_f32_e32 v55, v56, v68
	v_mul_f32_e32 v55, 0x3fb8aa3b, v55
	v_exp_f32_e32 v70, v55
	v_sub_f32_e32 v55, v57, v68
	v_sub_f32_e32 v57, v59, v68
	v_mul_f32_e32 v57, 0x3fb8aa3b, v57
	v_mul_f32_e32 v55, 0x3fb8aa3b, v55
	v_exp_f32_e32 v59, v57
	v_sub_f32_e32 v57, v60, v68
	v_exp_f32_e32 v71, v55
	v_sub_f32_e32 v55, v58, v68
	v_mul_f32_e32 v57, 0x3fb8aa3b, v57
	v_sub_f32_e32 v58, v61, v68
	v_exp_f32_e32 v57, v57
	v_mul_f32_e32 v58, 0x3fb8aa3b, v58
	v_exp_f32_e32 v58, v58
	v_mul_f32_e32 v55, 0x3fb8aa3b, v55
	v_exp_f32_e32 v72, v55
	v_cndmask_b32_e64 v60, 0, v57, s[0:1]
	v_sub_f32_e32 v57, v62, v68
	v_add_f32_e32 v56, 0, v70
	v_cndmask_b32_e64 v61, 0, v58, s[0:1]
	v_mul_f32_e32 v57, 0x3fb8aa3b, v57
	v_sub_f32_e32 v58, v63, v68
	v_add_f32_e32 v56, v56, v71
	v_exp_f32_e32 v57, v57
	v_mul_f32_e32 v58, 0x3fb8aa3b, v58
	v_add_f32_e32 v56, v56, v72
	v_exp_f32_e32 v58, v58
	v_add_f32_e32 v56, v56, v59
	v_add_f32_e32 v56, v56, v60
	v_add_f32_e32 v56, v56, v61
	v_cndmask_b32_e64 v62, 0, v57, s[0:1]
	v_add_f32_e32 v56, v56, v62
	v_cndmask_b32_e64 v63, 0, v58, s[0:1]
	v_add_f32_e32 v57, v56, v63
	v_mov_b32_e32 v58, v57
	s_nop 1
	v_permlane16_swap_b32_e32 v57, v58
	v_add_f32_e32 v58, v57, v58
	v_mov_b32_e32 v68, v58
	s_nop 1
	v_permlane32_swap_b32_e32 v58, v68
	v_add_f32_e32 v68, v58, v68
	v_div_scale_f32 v69, s[6:7], v68, v68, 1.0
	v_rcp_f32_e32 v73, v69
	s_nop 0
	v_fma_f32 v75, -v69, v73, 1.0
	v_fmac_f32_e32 v73, v75, v73
	v_div_scale_f32 v75, vcc, 1.0, v68, 1.0
	v_mul_f32_e32 v92, v75, v73
	v_fma_f32 v93, -v69, v92, v75
	v_fmac_f32_e32 v92, v93, v73
	v_fma_f32 v69, -v69, v92, v75
	v_div_fmas_f32 v69, v69, v73, v92
	v_div_fixup_f32 v68, v69, v68, 1.0
	v_mul_f32_e32 v69, v68, v70
	v_mov_b32_e32 v75, 0xbb23d70a
	v_mov_b32_e32 v73, 0x3b23d70a
	v_fmaak_f32 v92, v68, v70, 0xbb23d70a
	v_fmaak_f32 v70, v68, v70, 0x3b23d70a
	v_cmp_lt_f32_e32 vcc, v69, v75
	v_fmaak_f32 v93, v68, v60, 0xbb23d70a
	s_nop 0
	v_cndmask_b32_e32 v70, 0, v70, vcc
	v_cmp_gt_f32_e32 vcc, v69, v73
	s_nop 1
	v_cndmask_b32_e32 v69, v70, v92, vcc
	v_mul_f32_e32 v92, v68, v60
	v_fmaak_f32 v60, v68, v60, 0x3b23d70a
	v_cmp_lt_f32_e32 vcc, v92, v75
	v_max_f32_e32 v70, 0xf149f2ca, v69
	s_nop 0
	v_cndmask_b32_e32 v60, 0, v60, vcc
	v_cmp_gt_f32_e32 vcc, v92, v73
	s_nop 1
	v_cndmask_b32_e32 v92, v60, v93, vcc
	v_max_f32_e32 v60, v70, v92
	v_cndmask_b32_e64 v60, v70, v60, s[0:1]
	v_mul_f32_e32 v70, v68, v71
	v_fmaak_f32 v93, v68, v71, 0xbb23d70a
	v_fmaak_f32 v71, v68, v71, 0x3b23d70a
	v_cmp_lt_f32_e32 vcc, v70, v75
	s_nop 1
	v_cndmask_b32_e32 v71, 0, v71, vcc
	v_cmp_gt_f32_e32 vcc, v70, v73
	s_nop 1
	v_cndmask_b32_e32 v70, v71, v93, vcc
	v_mul_f32_e32 v71, v68, v61
	v_fmaak_f32 v93, v68, v61, 0xbb23d70a
	v_fmaak_f32 v61, v68, v61, 0x3b23d70a
	v_cmp_lt_f32_e32 vcc, v71, v75
	v_max_f32_e32 v60, v60, v70
	s_nop 0
	v_cndmask_b32_e32 v61, 0, v61, vcc
	v_cmp_gt_f32_e32 vcc, v71, v73
	s_nop 1
	v_cndmask_b32_e32 v71, v61, v93, vcc
	v_max_f32_e32 v61, v60, v71
	v_cndmask_b32_e64 v60, v60, v61, s[0:1]
	v_mul_f32_e32 v61, v68, v72
	v_fmaak_f32 v93, v68, v72, 0xbb23d70a
	v_fmaak_f32 v72, v68, v72, 0x3b23d70a
	v_cmp_lt_f32_e32 vcc, v61, v75
	s_nop 1
	v_cndmask_b32_e32 v72, 0, v72, vcc
	v_cmp_gt_f32_e32 vcc, v61, v73
	v_mul_f32_e32 v61, v68, v62
	s_nop 0
	v_cndmask_b32_e32 v72, v72, v93, vcc
	v_fmaak_f32 v93, v68, v62, 0xbb23d70a
	v_fmaak_f32 v62, v68, v62, 0x3b23d70a
	v_cmp_lt_f32_e32 vcc, v61, v75
	v_max_f32_e32 v60, v60, v72
	s_nop 0
	v_cndmask_b32_e32 v62, 0, v62, vcc
	v_cmp_gt_f32_e32 vcc, v61, v73
	s_nop 1
	v_cndmask_b32_e32 v62, v62, v93, vcc
	v_max_f32_e32 v61, v60, v62
	v_cndmask_b32_e64 v60, v60, v61, s[0:1]
	v_mul_f32_e32 v61, v68, v59
	v_fmaak_f32 v93, v68, v59, 0xbb23d70a
	v_fmaak_f32 v59, v68, v59, 0x3b23d70a
	v_cmp_lt_f32_e32 vcc, v61, v75
	s_nop 1
	v_cndmask_b32_e32 v59, 0, v59, vcc
	v_cmp_gt_f32_e32 vcc, v61, v73
	s_nop 1
	v_cndmask_b32_e32 v93, v59, v93, vcc
	v_max_f32_e32 v59, v60, v93
	v_mul_f32_e32 v60, v68, v63
	v_cmp_gt_f32_e32 vcc, v60, v73
	v_fmac_f32_e32 v73, v68, v63
	v_cmp_lt_f32_e64 s[6:7], v60, v75
	v_fmac_f32_e32 v75, v68, v63
	s_nop 0
	v_cndmask_b32_e64 v60, 0, v73, s[6:7]
	v_cndmask_b32_e32 v63, v60, v75, vcc
	v_max_f32_e32 v60, v59, v63
	v_cndmask_b32_e64 v60, v59, v60, s[0:1]
	v_mov_b32_e32 v61, v60
	s_nop 1
	v_permlane16_swap_b32_e32 v60, v61
	v_max_f32_e32 v61, v60, v61
	v_mov_b32_e32 v74, v61
	s_nop 1
	v_permlane32_swap_b32_e32 v61, v74
	v_max_f32_e32 v74, v61, v74
	v_sub_f32_e32 v61, v69, v74
	v_mul_f32_e32 v61, 0x3fb8aa3b, v61
	v_exp_f32_e32 v69, v61
	v_sub_f32_e32 v61, v92, v74
	v_mul_f32_e32 v61, 0x3fb8aa3b, v61
	v_exp_f32_e32 v75, v61
	v_sub_f32_e32 v70, v70, v74
	v_sub_f32_e32 v71, v71, v74
	v_mul_f32_e32 v70, 0x3fb8aa3b, v70
	v_mul_f32_e32 v71, 0x3fb8aa3b, v71
	v_exp_f32_e32 v70, v70
	v_exp_f32_e32 v71, v71
	v_sub_f32_e32 v72, v72, v74
	v_sub_f32_e32 v62, v62, v74
	v_mul_f32_e32 v72, 0x3fb8aa3b, v72
	v_mul_f32_e32 v62, 0x3fb8aa3b, v62
	v_add_f32_e32 v73, 0, v69
	v_cndmask_b32_e64 v75, 0, v75, s[0:1]
	v_exp_f32_e32 v72, v72
	v_exp_f32_e32 v62, v62
	v_sub_f32_e32 v84, v93, v74
	v_sub_f32_e32 v63, v63, v74
	v_add_f32_e32 v73, v73, v75
	v_mul_f32_e32 v84, 0x3fb8aa3b, v84
	v_mul_f32_e32 v63, 0x3fb8aa3b, v63
	v_add_f32_e32 v73, v73, v70
	v_cndmask_b32_e64 v71, 0, v71, s[0:1]
	v_exp_f32_e32 v84, v84
	v_exp_f32_e32 v63, v63
	v_add_f32_e32 v73, v73, v71
	v_add_f32_e32 v73, v73, v72
	v_cndmask_b32_e64 v74, 0, v62, s[0:1]
	v_add_f32_e32 v62, v73, v74
	v_add_f32_e32 v62, v62, v84
	v_cndmask_b32_e64 v73, 0, v63, s[0:1]
	v_add_f32_e32 v85, v62, v73
	v_mov_b32_e32 v66, v85
	s_nop 1
	v_permlane16_swap_b32_e32 v85, v66
	v_add_f32_e32 v66, v85, v66
	v_mov_b32_e32 v67, v66
	s_nop 1
	v_permlane32_swap_b32_e32 v66, v67
	v_add_f32_e32 v66, v66, v67
	v_div_scale_f32 v67, s[6:7], v66, v66, 1.0
	v_rcp_f32_e32 v78, v67
	s_nop 0
	v_fma_f32 v68, -v67, v78, 1.0
	v_fmac_f32_e32 v78, v68, v78
	v_div_scale_f32 v68, vcc, 1.0, v66, 1.0
	v_mul_f32_e32 v77, v68, v78
	v_fma_f32 v79, -v67, v77, v68
	v_fmac_f32_e32 v77, v79, v78
	v_fma_f32 v67, -v67, v77, v68
	v_div_fmas_f32 v67, v67, v78, v77
	v_div_fixup_f32 v66, v67, v66, 1.0
	v_mov_b32_e32 v67, 0xbd4ccccd
	v_fmaak_f32 v68, v66, v69, 0xbd4ccccd
	v_fmaak_f32 v69, v66, v70, 0xbd4ccccd
	v_fmaak_f32 v70, v66, v72, 0xbd4ccccd
	v_fmaak_f32 v75, v66, v75, 0xbd4ccccd
	v_fmaak_f32 v71, v66, v71, 0xbd4ccccd
	v_fmaak_f32 v74, v66, v74, 0xbd4ccccd
	v_mul_f32_e32 v70, 0x4038aa3b, v70
	v_fmaak_f32 v72, v66, v84, 0xbd4ccccd
	v_mul_f32_e32 v75, 0x4038aa3b, v75
	v_mul_f32_e32 v71, 0x4038aa3b, v71
	v_mul_f32_e32 v74, 0x4038aa3b, v74
	v_fmac_f32_e32 v67, v66, v73
	v_mul_f32_e32 v68, 0x4038aa3b, v68
	v_mul_f32_e32 v69, 0x4038aa3b, v69
	v_mul_f32_e32 v72, 0x4038aa3b, v72
	v_cndmask_b32_e64 v75, 0, v75, s[0:1]
	v_cndmask_b32_e64 v71, 0, v71, s[0:1]
	v_cndmask_b32_e64 v74, 0, v74, s[0:1]
	v_mul_f32_e32 v66, 0x4038aa3b, v67
	v_cvt_pk_bf16_f32 v67, v70, v72
	v_add_u32_e32 v70, v76, v198
	v_cndmask_b32_e64 v73, 0, v66, s[0:1]
	v_cndmask_b32_e64 v74, v74, 1.0, s[4:5]
	v_cndmask_b32_e64 v75, v75, 1.0, s[4:5]
	v_cndmask_b32_e64 v71, v71, 1.0, s[4:5]
	v_cvt_pk_bf16_f32 v66, v68, v69
	v_cvt_pk_bf16_f32 v68, v75, v71
	v_cvt_pk_bf16_f32 v69, v74, v73
	ds_write_b128 v70, v[66:69]
	s_waitcnt lgkmcnt(0)
	v_readfirstlane_b32 s47, v200
	s_nop 3
	s_lshl_b32 s15, s47, 2
	s_add_i32 s15, s15, 0x26800
	v_mov_b32_e32 v7, s15
	v_mov_b32_e32 v8, 1
	ds_write_b32 v7, v8
	s_mov_b32 s46, 0
.LBB0_3:
	s_add_i32 s14, s47, s46
	s_and_b32 s14, s14, 7
	s_lshl_b32 s13, s14, 25
	s_lshl_b32 s15, s14, 10
	v_add_u32_e32 v9, s15, v203
	s_lshl_b32 s15, s14, 2
	s_add_i32 s15, s15, 0x26800
	v_mov_b32_e32 v7, s15
.Lflag_spin:
	ds_read_b32 v8, v7
	s_waitcnt lgkmcnt(0)
	v_readfirstlane_b32 s15, v8
	s_nop 3
	s_cmp_eq_u32 s15, 1
	s_cbranch_scc1 .Lflag_go
	s_sleep 1
	s_branch .Lflag_spin
.Lflag_go:
	ds_read_b128 v[70:73], v9
	v_add_u32_e32 v132, s13, v220
	s_add_i32 s46, s46, 1
	s_cmp_eq_u32 s46, 8
	s_waitcnt lgkmcnt(0)
	v_mfma_f32_16x16x32_bf16 v[66:69], v[144:147], v[70:73], 0
	v_add_u32_e32 v133, 0x4000, v132
	v_add_u32_e32 v134, 0x8000, v132
	v_add_u32_e32 v135, 0xc000, v132
	v_mfma_f32_16x16x32_bf16 v[74:77], v[148:151], v[70:73], 0
	v_add_u32_e32 v136, 0x10000, v132
	s_nop 2
	v_exp_f32_e32 v66, v66
	v_exp_f32_e32 v67, v67
	v_mfma_f32_16x16x32_bf16 v[78:81], v[152:155], v[70:73], 0
	v_exp_f32_e32 v68, v68
	v_exp_f32_e32 v69, v69
	v_exp_f32_e32 v74, v74
	v_mfma_f32_16x16x32_bf16 v[82:85], v[156:159], v[70:73], 0
	v_exp_f32_e32 v75, v75
	v_exp_f32_e32 v76, v76
	v_exp_f32_e32 v77, v77
	v_mfma_f32_16x16x32_bf16 v[86:89], v[160:163], v[70:73], 0
	v_exp_f32_e32 v78, v78
	v_exp_f32_e32 v79, v79
	v_exp_f32_e32 v80, v80
	v_mfma_f32_16x16x32_bf16 v[90:93], v[164:167], v[70:73], 0
	v_exp_f32_e32 v81, v81
	v_exp_f32_e32 v82, v82
	v_exp_f32_e32 v83, v83
	v_mfma_f32_16x16x32_bf16 v[94:97], v[168:171], v[70:73], 0
	v_exp_f32_e32 v84, v84
	v_exp_f32_e32 v85, v85
	v_exp_f32_e32 v86, v86
	v_mfma_f32_16x16x32_bf16 v[98:101], v[172:175], v[70:73], 0
	v_exp_f32_e32 v87, v87
	v_exp_f32_e32 v88, v88
	v_exp_f32_e32 v89, v89
	v_mfma_f32_16x16x32_bf16 v[102:105], v[176:179], v[70:73], 0
	v_exp_f32_e32 v90, v90
	v_exp_f32_e32 v91, v91
	v_exp_f32_e32 v92, v92
	v_mfma_f32_16x16x32_bf16 v[108:111], v[180:183], v[70:73], 0
	v_exp_f32_e32 v93, v93
	v_exp_f32_e32 v94, v94
	v_exp_f32_e32 v95, v95
	v_mfma_f32_16x16x32_bf16 v[112:115], v[184:187], v[70:73], 0
	v_exp_f32_e32 v96, v96
	v_exp_f32_e32 v97, v97
	v_exp_f32_e32 v98, v98
	v_mfma_f32_16x16x32_bf16 v[116:119], v[188:191], v[70:73], 0
	v_exp_f32_e32 v99, v99
	v_exp_f32_e32 v100, v100
	v_exp_f32_e32 v101, v101
	v_mfma_f32_16x16x32_bf16 v[120:123], v[232:235], v[70:73], 0
	v_exp_f32_e32 v102, v102
	v_exp_f32_e32 v103, v103
	v_exp_f32_e32 v104, v104
	v_mfma_f32_16x16x32_bf16 v[124:127], v[236:239], v[70:73], 0
	v_exp_f32_e32 v105, v105
	v_exp_f32_e32 v108, v108
	v_exp_f32_e32 v109, v109
	v_mfma_f32_16x16x32_bf16 v[128:131], v[240:243], v[70:73], 0
	v_exp_f32_e32 v110, v110
	v_exp_f32_e32 v111, v111
	v_exp_f32_e32 v112, v112
	v_mfma_f32_16x16x32_bf16 v[70:73], v[244:247], v[70:73], 0
	v_exp_f32_e32 v113, v113
	v_exp_f32_e32 v114, v114
	v_exp_f32_e32 v115, v115
	v_exp_f32_e32 v116, v116
	v_exp_f32_e32 v117, v117
	v_exp_f32_e32 v118, v118
	v_exp_f32_e32 v119, v119
	v_exp_f32_e32 v120, v120
	v_exp_f32_e32 v121, v121
	v_exp_f32_e32 v122, v122
	v_exp_f32_e32 v123, v123
	v_exp_f32_e32 v124, v124
	v_exp_f32_e32 v125, v125
	v_exp_f32_e32 v126, v126
	v_exp_f32_e32 v127, v127
	v_exp_f32_e32 v128, v128
	v_exp_f32_e32 v129, v129
	v_exp_f32_e32 v130, v130
	v_exp_f32_e32 v131, v131
	v_exp_f32_e32 v70, v70
	v_exp_f32_e32 v71, v71
	v_exp_f32_e32 v72, v72
	v_exp_f32_e32 v73, v73
	v_pk_add_f32 v[66:67], v[66:67], 1.0 op_sel_hi:[1,0]
	v_pk_add_f32 v[68:69], v[68:69], 1.0 op_sel_hi:[1,0]
	v_pk_add_f32 v[74:75], v[74:75], 1.0 op_sel_hi:[1,0]
	v_pk_add_f32 v[76:77], v[76:77], 1.0 op_sel_hi:[1,0]
	v_pk_add_f32 v[78:79], v[78:79], 1.0 op_sel_hi:[1,0]
	v_pk_add_f32 v[80:81], v[80:81], 1.0 op_sel_hi:[1,0]
	v_pk_add_f32 v[82:83], v[82:83], 1.0 op_sel_hi:[1,0]
	v_pk_add_f32 v[84:85], v[84:85], 1.0 op_sel_hi:[1,0]
	v_pk_add_f32 v[86:87], v[86:87], 1.0 op_sel_hi:[1,0]
	v_pk_add_f32 v[88:89], v[88:89], 1.0 op_sel_hi:[1,0]
	v_pk_add_f32 v[90:91], v[90:91], 1.0 op_sel_hi:[1,0]
	v_pk_add_f32 v[92:93], v[92:93], 1.0 op_sel_hi:[1,0]
	v_pk_add_f32 v[94:95], v[94:95], 1.0 op_sel_hi:[1,0]
	v_pk_add_f32 v[96:97], v[96:97], 1.0 op_sel_hi:[1,0]
	v_pk_add_f32 v[98:99], v[98:99], 1.0 op_sel_hi:[1,0]
	v_pk_add_f32 v[100:101], v[100:101], 1.0 op_sel_hi:[1,0]
	v_pk_add_f32 v[102:103], v[102:103], 1.0 op_sel_hi:[1,0]
	v_pk_add_f32 v[104:105], v[104:105], 1.0 op_sel_hi:[1,0]
	v_rcp_f32_e32 v66, v66
	v_rcp_f32_e32 v67, v67
	v_rcp_f32_e32 v68, v68
	v_rcp_f32_e32 v69, v69
	v_pk_add_f32 v[108:109], v[108:109], 1.0 op_sel_hi:[1,0]
	v_pk_add_f32 v[110:111], v[110:111], 1.0 op_sel_hi:[1,0]
	v_pk_add_f32 v[112:113], v[112:113], 1.0 op_sel_hi:[1,0]
	v_pk_add_f32 v[114:115], v[114:115], 1.0 op_sel_hi:[1,0]
	v_pk_add_f32 v[116:117], v[116:117], 1.0 op_sel_hi:[1,0]
	v_pk_add_f32 v[118:119], v[118:119], 1.0 op_sel_hi:[1,0]
	v_pk_add_f32 v[120:121], v[120:121], 1.0 op_sel_hi:[1,0]
	v_pk_add_f32 v[122:123], v[122:123], 1.0 op_sel_hi:[1,0]
	v_pk_add_f32 v[124:125], v[124:125], 1.0 op_sel_hi:[1,0]
	v_pk_add_f32 v[126:127], v[126:127], 1.0 op_sel_hi:[1,0]
	v_pk_add_f32 v[128:129], v[128:129], 1.0 op_sel_hi:[1,0]
	v_pk_add_f32 v[130:131], v[130:131], 1.0 op_sel_hi:[1,0]
	v_add_f32_e32 v140, 1.0, v70
	v_add_f32_e32 v141, 1.0, v71
	v_add_f32_e32 v142, 1.0, v72
	v_add_f32_e32 v143, 1.0, v73
	v_rcp_f32_e32 v70, v74
	v_rcp_f32_e32 v71, v75
	v_rcp_f32_e32 v72, v76
	v_rcp_f32_e32 v73, v77
	v_rcp_f32_e32 v74, v78
	v_rcp_f32_e32 v75, v79
	v_rcp_f32_e32 v76, v80
	v_rcp_f32_e32 v77, v81
	v_rcp_f32_e32 v78, v82
	v_rcp_f32_e32 v79, v83
	v_rcp_f32_e32 v80, v84
	v_rcp_f32_e32 v81, v85
	v_rcp_f32_e32 v82, v86
	v_rcp_f32_e32 v83, v87
	v_rcp_f32_e32 v84, v88
	v_rcp_f32_e32 v85, v89
	v_rcp_f32_e32 v86, v90
	v_rcp_f32_e32 v87, v91
	v_rcp_f32_e32 v88, v92
	v_rcp_f32_e32 v89, v93
	v_rcp_f32_e32 v90, v94
	v_rcp_f32_e32 v91, v95
	v_rcp_f32_e32 v92, v96
	v_rcp_f32_e32 v93, v97
	v_rcp_f32_e32 v94, v98
	v_rcp_f32_e32 v95, v99
	v_rcp_f32_e32 v96, v100
	v_rcp_f32_e32 v97, v101
	v_rcp_f32_e32 v98, v102
	v_rcp_f32_e32 v99, v103
	v_rcp_f32_e32 v100, v104
	v_rcp_f32_e32 v101, v105
	v_rcp_f32_e32 v102, v108
	v_rcp_f32_e32 v103, v109
	v_rcp_f32_e32 v104, v110
	v_rcp_f32_e32 v105, v111
	v_rcp_f32_e32 v108, v112
	v_rcp_f32_e32 v109, v113
	v_rcp_f32_e32 v110, v114
	v_rcp_f32_e32 v111, v115
	v_rcp_f32_e32 v112, v116
	v_rcp_f32_e32 v113, v117
	v_rcp_f32_e32 v114, v118
	v_rcp_f32_e32 v115, v119
	v_rcp_f32_e32 v116, v120
	v_rcp_f32_e32 v117, v121
	v_rcp_f32_e32 v118, v122
	v_rcp_f32_e32 v119, v123
	v_rcp_f32_e32 v120, v124
	v_rcp_f32_e32 v121, v125
	v_rcp_f32_e32 v122, v126
	v_rcp_f32_e32 v123, v127
	v_rcp_f32_e32 v124, v128
	v_rcp_f32_e32 v125, v129
	v_rcp_f32_e32 v126, v130
	v_rcp_f32_e32 v127, v131
	v_rcp_f32_e32 v128, v140
	v_rcp_f32_e32 v129, v141
	v_rcp_f32_e32 v130, v142
	v_rcp_f32_e32 v131, v143
	v_pk_fma_f32 v[66:67], v[66:67], -2.0, 1.0 op_sel_hi:[1,0,0]
	v_pk_fma_f32 v[68:69], v[68:69], -2.0, 1.0 op_sel_hi:[1,0,0]
	v_pk_fma_f32 v[70:71], v[70:71], -2.0, 1.0 op_sel_hi:[1,0,0]
	v_pk_fma_f32 v[72:73], v[72:73], -2.0, 1.0 op_sel_hi:[1,0,0]
	v_pk_fma_f32 v[74:75], v[74:75], -2.0, 1.0 op_sel_hi:[1,0,0]
	v_pk_fma_f32 v[76:77], v[76:77], -2.0, 1.0 op_sel_hi:[1,0,0]
	v_pk_fma_f32 v[78:79], v[78:79], -2.0, 1.0 op_sel_hi:[1,0,0]
	v_pk_fma_f32 v[80:81], v[80:81], -2.0, 1.0 op_sel_hi:[1,0,0]
	v_pk_fma_f32 v[82:83], v[82:83], -2.0, 1.0 op_sel_hi:[1,0,0]
	v_pk_fma_f32 v[84:85], v[84:85], -2.0, 1.0 op_sel_hi:[1,0,0]
	v_pk_fma_f32 v[86:87], v[86:87], -2.0, 1.0 op_sel_hi:[1,0,0]
	v_pk_fma_f32 v[88:89], v[88:89], -2.0, 1.0 op_sel_hi:[1,0,0]
	v_pk_fma_f32 v[90:91], v[90:91], -2.0, 1.0 op_sel_hi:[1,0,0]
	v_pk_fma_f32 v[92:93], v[92:93], -2.0, 1.0 op_sel_hi:[1,0,0]
	v_pk_fma_f32 v[94:95], v[94:95], -2.0, 1.0 op_sel_hi:[1,0,0]
	v_pk_fma_f32 v[96:97], v[96:97], -2.0, 1.0 op_sel_hi:[1,0,0]
	v_pk_fma_f32 v[98:99], v[98:99], -2.0, 1.0 op_sel_hi:[1,0,0]
	v_pk_fma_f32 v[100:101], v[100:101], -2.0, 1.0 op_sel_hi:[1,0,0]
	ds_write_b128 v214, v[66:69]
	ds_write_b128 v214, v[70:73] offset:64
	ds_write_b128 v214, v[74:77] offset:128
	ds_write_b128 v214, v[78:81] offset:192
	ds_write_b128 v214, v[82:85] offset:256
	ds_write_b128 v214, v[86:89] offset:320
	ds_write_b128 v214, v[90:93] offset:384
	ds_write_b128 v214, v[94:97] offset:448
	v_pk_fma_f32 v[102:103], v[102:103], -2.0, 1.0 op_sel_hi:[1,0,0]
	v_pk_fma_f32 v[104:105], v[104:105], -2.0, 1.0 op_sel_hi:[1,0,0]
	v_pk_fma_f32 v[108:109], v[108:109], -2.0, 1.0 op_sel_hi:[1,0,0]
	v_pk_fma_f32 v[110:111], v[110:111], -2.0, 1.0 op_sel_hi:[1,0,0]
	v_pk_fma_f32 v[112:113], v[112:113], -2.0, 1.0 op_sel_hi:[1,0,0]
	v_pk_fma_f32 v[114:115], v[114:115], -2.0, 1.0 op_sel_hi:[1,0,0]
	v_pk_fma_f32 v[116:117], v[116:117], -2.0, 1.0 op_sel_hi:[1,0,0]
	v_pk_fma_f32 v[118:119], v[118:119], -2.0, 1.0 op_sel_hi:[1,0,0]
	v_pk_fma_f32 v[120:121], v[120:121], -2.0, 1.0 op_sel_hi:[1,0,0]
	v_pk_fma_f32 v[122:123], v[122:123], -2.0, 1.0 op_sel_hi:[1,0,0]
	v_pk_fma_f32 v[124:125], v[124:125], -2.0, 1.0 op_sel_hi:[1,0,0]
	v_pk_fma_f32 v[126:127], v[126:127], -2.0, 1.0 op_sel_hi:[1,0,0]
	v_pk_fma_f32 v[128:129], v[128:129], -2.0, 1.0 op_sel_hi:[1,0,0]
	v_pk_fma_f32 v[130:131], v[130:131], -2.0, 1.0 op_sel_hi:[1,0,0]
	ds_read_b128 v[66:69], v215
	ds_read_b128 v[70:73], v215 offset:1056
	ds_read_b128 v[74:77], v215 offset:2112
	ds_read_b128 v[78:81], v215 offset:3168
	ds_read_b128 v[82:85], v215 offset:4224
	ds_read_b128 v[86:89], v215 offset:5280
	ds_read_b128 v[90:93], v215 offset:6336
	ds_read_b128 v[94:97], v215 offset:7392
	ds_write_b128 v214, v[98:101]
	ds_write_b128 v214, v[102:105] offset:64
	ds_write_b128 v214, v[108:111] offset:128
	ds_write_b128 v214, v[112:115] offset:192
	ds_write_b128 v214, v[116:119] offset:256
	ds_write_b128 v214, v[120:123] offset:320
	ds_write_b128 v214, v[124:127] offset:384
	ds_write_b128 v214, v[128:131] offset:448
	ds_read_b128 v[98:101], v215
	ds_read_b128 v[102:105], v215 offset:1056
	ds_read_b128 v[108:111], v215 offset:2112
	ds_read_b128 v[112:115], v215 offset:3168
	ds_read_b128 v[116:119], v215 offset:4224
	ds_read_b128 v[120:123], v215 offset:5280
	ds_read_b128 v[124:127], v215 offset:6336
	ds_read_b128 v[128:131], v215 offset:7392
	v_add_u32_e32 v137, 0x14000, v132
	v_add_u32_e32 v138, 0x18000, v132
	v_add_u32_e32 v139, 0x1c000, v132
	s_waitcnt lgkmcnt(14)
	buffer_store_dwordx4 v[66:69], v132, s[8:11], 0 offen sc0 nt sc1
	buffer_store_dwordx4 v[70:73], v133, s[8:11], 0 offen sc0 nt sc1
	buffer_store_dwordx4 v[74:77], v134, s[8:11], 0 offen sc0 nt sc1
	buffer_store_dwordx4 v[78:81], v135, s[8:11], 0 offen sc0 nt sc1
	buffer_store_dwordx4 v[82:85], v136, s[8:11], 0 offen sc0 nt sc1
	buffer_store_dwordx4 v[86:89], v137, s[8:11], 0 offen sc0 nt sc1
	buffer_store_dwordx4 v[90:93], v138, s[8:11], 0 offen sc0 nt sc1
	buffer_store_dwordx4 v[94:97], v139, s[8:11], 0 offen sc0 nt sc1
	s_waitcnt lgkmcnt(7)
	buffer_store_dwordx4 v[98:101], v132, s[8:11], 0 offen offset:512 sc0 nt sc1
	s_waitcnt lgkmcnt(6)
	buffer_store_dwordx4 v[102:105], v133, s[8:11], 0 offen offset:512 sc0 nt sc1
	s_waitcnt lgkmcnt(5)
	buffer_store_dwordx4 v[108:111], v134, s[8:11], 0 offen offset:512 sc0 nt sc1
	s_waitcnt lgkmcnt(4)
	buffer_store_dwordx4 v[112:115], v135, s[8:11], 0 offen offset:512 sc0 nt sc1
	s_waitcnt lgkmcnt(3)
	buffer_store_dwordx4 v[116:119], v136, s[8:11], 0 offen offset:512 sc0 nt sc1
	s_waitcnt lgkmcnt(2)
	buffer_store_dwordx4 v[120:123], v137, s[8:11], 0 offen offset:512 sc0 nt sc1
	s_waitcnt lgkmcnt(1)
	buffer_store_dwordx4 v[124:127], v138, s[8:11], 0 offen offset:512 sc0 nt sc1
	s_waitcnt lgkmcnt(0)
	buffer_store_dwordx4 v[128:131], v139, s[8:11], 0 offen offset:512 sc0 nt sc1
	s_cbranch_scc0 .LBB0_3
	s_endpgm

	.amdhsa_kernel _Z12fused_kernelPKfS0_Pf
		.amdhsa_group_segment_fixed_size 157760
		.amdhsa_private_segment_fixed_size 0
		.amdhsa_kernarg_size 24
		.amdhsa_user_sgpr_count 2
		.amdhsa_user_sgpr_dispatch_ptr 0
		.amdhsa_user_sgpr_queue_ptr 0
		.amdhsa_user_sgpr_kernarg_segment_ptr 1
		.amdhsa_user_sgpr_dispatch_id 0
		.amdhsa_user_sgpr_kernarg_preload_length 0
		.amdhsa_user_sgpr_kernarg_preload_offset 0
		.amdhsa_user_sgpr_private_segment_size 0
		.amdhsa_uses_dynamic_stack 0
		.amdhsa_enable_private_segment 0
		.amdhsa_system_sgpr_workgroup_id_x 1
		.amdhsa_system_sgpr_workgroup_id_y 0
		.amdhsa_system_sgpr_workgroup_id_z 0
		.amdhsa_system_sgpr_workgroup_info 0
		.amdhsa_system_vgpr_workitem_id 0
		.amdhsa_next_free_vgpr 248
		.amdhsa_next_free_sgpr 96
		.amdhsa_accum_offset 248
		.amdhsa_reserve_vcc 1
		.amdhsa_float_round_mode_32 0
		.amdhsa_float_round_mode_16_64 0
		.amdhsa_float_denorm_mode_32 3
		.amdhsa_float_denorm_mode_16_64 3
		.amdhsa_dx10_clamp 1
		.amdhsa_ieee_mode 1
		.amdhsa_fp16_overflow 0
		.amdhsa_tg_split 0
		.amdhsa_exception_fp_ieee_invalid_op 0
		.amdhsa_exception_fp_denorm_src 0
		.amdhsa_exception_fp_ieee_div_zero 0
		.amdhsa_exception_fp_ieee_overflow 0
		.amdhsa_exception_fp_ieee_underflow 0
		.amdhsa_exception_fp_ieee_inexact 0
		.amdhsa_exception_int_div_zero 0
	.end_amdhsa_kernel

amdhsa.kernels:
  - .agpr_count:     0
    .args:
      - .actual_access:  read_only
        .address_space:  global
        .offset:         0
        .size:           8
        .value_kind:     global_buffer
      - .actual_access:  read_only
        .address_space:  global
        .offset:         8
        .size:           8
        .value_kind:     global_buffer
      - .actual_access:  write_only
        .address_space:  global
        .offset:         16
        .size:           8
        .value_kind:     global_buffer
    .group_segment_fixed_size: 157760
    .kernarg_segment_align: 8
    .kernarg_segment_size: 24
    .language:       OpenCL C
    .language_version:
      - 2
      - 0
    .max_flat_workgroup_size: 512
    .name:           _Z12fused_kernelPKfS0_Pf
    .private_segment_fixed_size: 0
    .sgpr_count:     34
    .sgpr_spill_count: 0
    .symbol:         _Z12fused_kernelPKfS0_Pf.kd
    .uniform_work_group_size: 1
    .uses_dynamic_stack: false
    .vgpr_count:     248
    .vgpr_spill_count: 0
    .wavefront_size: 64
